# speedup vs baseline: 1.0787x; 1.0062x over previous
.LBB2_24:
	s_or_b64 exec, exec, s[0:1]
	v_and_b32_e32 v1, 31, v0
	v_lshlrev_b32_e32 v2, 2, v1
	v_lshl_or_b32 v2, s10, 7, v2
	v_or_b32_e32 v2, 0x1ee00, v2
	v_lshrrev_b32_e32 v158, 5, v156
	s_waitcnt lgkmcnt(0)
	s_barrier
	s_barrier
	ds_read_b32 v157, v2
	v_mul_u32_u24_e32 v2, 0x88, v1
	s_mul_i32 s0, s11, 0x4400
	v_lshlrev_b32_e32 v2, 1, v2
	v_lshlrev_b32_e32 v3, 4, v158
	v_mov_b32_e32 v138, v0
	v_add3_u32 v159, s0, v2, v3
	ds_read_b128 v[2:5], v159
	ds_read_b128 v[18:21], v159 offset:8704
	ds_read_b128 v[130:133], v159 offset:32
	s_waitcnt vmcnt(10) lgkmcnt(2)
	v_mfma_f32_32x32x16_f16 v[50:65], v[2:5], v[126:129], 0
	s_mov_b32 s4, 0xc060c00
	s_mov_b32 s5, 0xe400
	s_mulk_i32 s11, 0x2400
	s_lshl_b32 s0, s10, 6
	s_or_b32 s0, s11, s0
	s_add_i32 s0, s0, 0x11000
	v_lshl_or_b32 v1, v1, 1, s0
	s_waitcnt lgkmcnt(1)
	v_mfma_f32_32x32x16_f16 v[34:49], v[18:21], v[126:129], 0
	s_or_b32 s0, s8, 2
	s_ashr_i32 s1, s0, 31
	s_lshl_b64 s[0:1], s[0:1], 12
	s_add_u32 s0, s2, s0
	s_addc_u32 s1, s3, s1
	v_cmp_gt_u32_e32 vcc, 32, v156
	v_mfma_f32_32x32x16_f16 v[2:17], v[2:5], v[122:125], 0
	v_mfma_f32_32x32x16_f16 v[18:33], v[18:21], v[122:125], 0
	ds_read_b128 v[134:137], v159 offset:8736
	ds_read_b128 v[160:163], v159 offset:64
	s_waitcnt vmcnt(8) lgkmcnt(2)
	v_mfma_f32_32x32x16_f16 v[50:65], v[130:133], v[118:121], v[50:65]
	s_waitcnt lgkmcnt(1)
	v_mfma_f32_32x32x16_f16 v[34:49], v[134:137], v[118:121], v[34:49]
	v_mfma_f32_32x32x16_f16 v[2:17], v[130:133], v[114:117], v[2:17]
	v_mfma_f32_32x32x16_f16 v[18:33], v[134:137], v[114:117], v[18:33]
	ds_read_b128 v[130:133], v159 offset:8768
	ds_read_b128 v[134:137], v159 offset:96
	s_waitcnt vmcnt(6) lgkmcnt(2)
	v_mfma_f32_32x32x16_f16 v[50:65], v[160:163], v[110:113], v[50:65]
	s_waitcnt lgkmcnt(1)
	v_mfma_f32_32x32x16_f16 v[34:49], v[130:133], v[110:113], v[34:49]
	v_mfma_f32_32x32x16_f16 v[2:17], v[160:163], v[106:109], v[2:17]
	v_mfma_f32_32x32x16_f16 v[18:33], v[130:133], v[106:109], v[18:33]
	ds_read_b128 v[130:133], v159 offset:8800
	ds_read_b128 v[160:163], v159 offset:128
	s_waitcnt vmcnt(4) lgkmcnt(2)
	v_mfma_f32_32x32x16_f16 v[50:65], v[134:137], v[102:105], v[50:65]
	s_waitcnt lgkmcnt(1)
	v_mfma_f32_32x32x16_f16 v[34:49], v[130:133], v[102:105], v[34:49]
	v_mfma_f32_32x32x16_f16 v[2:17], v[134:137], v[98:101], v[2:17]
	v_mfma_f32_32x32x16_f16 v[18:33], v[130:133], v[98:101], v[18:33]
	ds_read_b128 v[130:133], v159 offset:8832
	ds_read_b128 v[134:137], v159 offset:160
	s_waitcnt vmcnt(3) lgkmcnt(2)
	v_mfma_f32_32x32x16_f16 v[50:65], v[160:163], v[94:97], v[50:65]
	s_waitcnt lgkmcnt(1)
	v_mfma_f32_32x32x16_f16 v[34:49], v[130:133], v[94:97], v[34:49]
	v_mfma_f32_32x32x16_f16 v[2:17], v[160:163], v[86:89], v[2:17]
	v_mfma_f32_32x32x16_f16 v[18:33], v[130:133], v[86:89], v[18:33]
	ds_read_b128 v[130:133], v159 offset:8864
	ds_read_b128 v[160:163], v159 offset:192
	s_waitcnt vmcnt(2) lgkmcnt(2)
	v_mfma_f32_32x32x16_f16 v[50:65], v[134:137], v[90:93], v[50:65]
	s_waitcnt lgkmcnt(1)
	v_mfma_f32_32x32x16_f16 v[34:49], v[130:133], v[90:93], v[34:49]
	v_mfma_f32_32x32x16_f16 v[2:17], v[134:137], v[78:81], v[2:17]
	v_mfma_f32_32x32x16_f16 v[18:33], v[130:133], v[78:81], v[18:33]
	ds_read_b128 v[130:133], v159 offset:8896
	ds_read_b128 v[164:167], v159 offset:224
	s_waitcnt vmcnt(1) lgkmcnt(2)
	v_mfma_f32_32x32x16_f16 v[50:65], v[160:163], v[82:85], v[50:65]
	s_waitcnt lgkmcnt(1)
	v_mfma_f32_32x32x16_f16 v[34:49], v[130:133], v[82:85], v[34:49]
	v_mfma_f32_32x32x16_f16 v[2:17], v[160:163], v[70:73], v[2:17]
	v_mfma_f32_32x32x16_f16 v[18:33], v[130:133], v[70:73], v[18:33]
	v_lshlrev_b32_e32 v130, 3, v138
	v_and_b32_e32 v168, 0x1f8, v130
	global_load_dwordx2 v[138:139], v168, s[0:1]
	global_load_dwordx2 v[134:135], v168, s[0:1] offset:512
	global_load_dwordx2 v[132:133], v168, s[0:1] offset:1024
	global_load_dwordx2 v[130:131], v168, s[0:1] offset:1536
	global_load_dwordx2 v[136:137], v168, s[0:1] offset:2048
	s_waitcnt vmcnt(5) lgkmcnt(0)
	v_mfma_f32_32x32x16_f16 v[50:65], v[164:167], v[74:77], v[50:65]
	v_mfma_f32_32x32x16_f16 v[2:17], v[164:167], v[66:69], v[2:17]
	s_nop 10
	v_cvt_pk_f16_f32 v57, v56, v57
	v_cvt_pk_f16_f32 v56, v54, v55
	v_cvt_pk_f16_f32 v55, v52, v53
	v_cvt_pk_f16_f32 v54, v50, v51
	v_perm_b32 v50, v240, v154, s42
	v_perm_b32 v51, v240, v154, s43
	v_perm_b32 v52, v240, v155, s42
	v_perm_b32 v53, v240, v155, s43
	v_pk_add_f16 v50, v50, s5 op_sel_hi:[1,0]
	v_pk_add_f16 v51, v51, s5 op_sel_hi:[1,0]
	v_pk_add_f16 v52, v52, s5 op_sel_hi:[1,0]
	v_pk_add_f16 v53, v53, s5 op_sel_hi:[1,0]
	v_cvt_pk_f16_f32 v65, v64, v65
	v_cvt_pk_f16_f32 v64, v62, v63
	v_cvt_pk_f16_f32 v63, v60, v61
	v_cvt_pk_f16_f32 v62, v58, v59
	v_mfma_f32_32x32x16_f16 v[2:17], v[50:53], v[54:57], v[2:17]
	v_perm_b32 v58, v240, v150, s42
	v_perm_b32 v59, v240, v150, s43
	v_perm_b32 v60, v240, v151, s42
	v_perm_b32 v61, v240, v151, s43
	v_pk_add_f16 v58, v58, s5 op_sel_hi:[1,0]
	v_pk_add_f16 v59, v59, s5 op_sel_hi:[1,0]
	v_pk_add_f16 v60, v60, s5 op_sel_hi:[1,0]
	v_pk_add_f16 v61, v61, s5 op_sel_hi:[1,0]
	s_nop 1
	v_mfma_f32_32x32x16_f16 v[2:17], v[58:61], v[62:65], v[2:17]
	ds_read_b128 v[160:163], v159 offset:8928
	v_perm_b32 v155, v240, v152, s43
	v_perm_b32 v164, v240, v153, s42
	s_waitcnt lgkmcnt(0)
	v_mfma_f32_32x32x16_f16 v[18:33], v[160:163], v[66:69], v[18:33]
	v_perm_b32 v154, v240, v152, s42
	v_perm_b32 v165, v240, v153, s43
	v_pk_add_f16 v152, v154, s5 op_sel_hi:[1,0]
	v_pk_add_f16 v153, v155, s5 op_sel_hi:[1,0]
	v_pk_add_f16 v154, v164, s5 op_sel_hi:[1,0]
	v_pk_add_f16 v155, v165, s5 op_sel_hi:[1,0]
	v_mfma_f32_32x32x16_f16 v[34:49], v[160:163], v[74:77], v[34:49]
	v_perm_b32 v151, v240, v148, s43
	v_perm_b32 v164, v240, v149, s42
	v_mfma_f32_32x32x16_f16 v[18:33], v[152:155], v[54:57], v[18:33]
	v_perm_b32 v150, v240, v148, s42
	v_perm_b32 v165, v240, v149, s43
	v_pk_add_f16 v148, v150, s5 op_sel_hi:[1,0]
	v_pk_add_f16 v149, v151, s5 op_sel_hi:[1,0]
	v_pk_add_f16 v150, v164, s5 op_sel_hi:[1,0]
	v_pk_add_f16 v151, v165, s5 op_sel_hi:[1,0]
	s_nop 2
	v_cvt_pk_f16_f32 v41, v40, v41
	v_cvt_pk_f16_f32 v40, v38, v39
	v_cvt_pk_f16_f32 v38, v34, v35
	v_cvt_pk_f16_f32 v39, v36, v37
	v_mfma_f32_32x32x16_f16 v[18:33], v[148:151], v[62:65], v[18:33]
	v_perm_b32 v34, v240, v146, s42
	v_perm_b32 v35, v240, v146, s43
	v_perm_b32 v36, v240, v147, s42
	v_perm_b32 v37, v240, v147, s43
	v_pk_add_f16 v34, v34, s5 op_sel_hi:[1,0]
	v_pk_add_f16 v35, v35, s5 op_sel_hi:[1,0]
	v_pk_add_f16 v36, v36, s5 op_sel_hi:[1,0]
	v_pk_add_f16 v37, v37, s5 op_sel_hi:[1,0]
	v_perm_b32 v146, v240, v144, s42
	v_perm_b32 v144, v240, v144, s43
	v_perm_b32 v147, v240, v145, s42
	v_perm_b32 v53, v240, v145, s43
	v_pk_add_f16 v50, v146, s5 op_sel_hi:[1,0]
	v_pk_add_f16 v51, v144, s5 op_sel_hi:[1,0]
	v_pk_add_f16 v52, v147, s5 op_sel_hi:[1,0]
	v_pk_add_f16 v53, v53, s5 op_sel_hi:[1,0]
	v_cvt_pk_f16_f32 v49, v48, v49
	v_cvt_pk_f16_f32 v48, v46, v47
	v_cvt_pk_f16_f32 v47, v44, v45
	v_mfma_f32_32x32x16_f16 v[2:17], v[34:37], v[38:41], v[2:17]
	v_cvt_pk_f16_f32 v46, v42, v43
	v_mfma_f32_32x32x16_f16 v[18:33], v[50:53], v[38:41], v[18:33]
	v_perm_b32 v34, v240, v140, s42
	v_perm_b32 v35, v240, v140, s43
	v_perm_b32 v36, v240, v141, s42
	v_perm_b32 v37, v240, v141, s43
	v_perm_b32 v42, v240, v142, s42
	v_perm_b32 v43, v240, v142, s43
	v_perm_b32 v44, v240, v143, s42
	v_perm_b32 v45, v240, v143, s43
	v_pk_add_f16 v34, v34, s5 op_sel_hi:[1,0]
	v_pk_add_f16 v35, v35, s5 op_sel_hi:[1,0]
	v_pk_add_f16 v36, v36, s5 op_sel_hi:[1,0]
	v_pk_add_f16 v37, v37, s5 op_sel_hi:[1,0]
	v_pk_add_f16 v42, v42, s5 op_sel_hi:[1,0]
	v_pk_add_f16 v43, v43, s5 op_sel_hi:[1,0]
	v_pk_add_f16 v44, v44, s5 op_sel_hi:[1,0]
	v_pk_add_f16 v45, v45, s5 op_sel_hi:[1,0]
	v_mfma_f32_32x32x16_f16 v[18:33], v[34:37], v[46:49], v[18:33]
	global_load_dwordx2 v[154:155], v168, s[0:1] offset:2560
	global_load_dwordx2 v[152:153], v168, s[0:1] offset:3072
	global_load_dwordx2 v[150:151], v168, s[0:1] offset:3584
	v_mov_b32_e32 v148, v0
	s_or_b32 s0, s8, 4
	s_ashr_i32 s1, s0, 31
	s_lshl_b64 s[0:1], s[0:1], 12
	v_mfma_f32_32x32x16_f16 v[2:17], v[42:45], v[46:49], v[2:17]
	s_nop 3
	v_add_f32_e32 v196, v157, v18
	v_mul_u32_u24_e32 v18, 0x120, v158
	v_lshl_add_u32 v158, v18, 1, v1
	v_cvt_f16_f32_e32 v1, v196
	v_add_f32_e32 v204, v157, v20
	v_add_f32_e32 v160, v157, v21
	v_add_f32_e32 v162, v157, v22
	s_nop 0
	v_add_f32_e32 v193, v157, v2
	v_add_f32_e32 v198, v157, v3
	v_cvt_pk_f16_f32 v2, v193, v198
	ds_write_b16 v158, v1 offset:4608
	v_add_f32_e32 v203, v157, v4
	v_add_f32_e32 v1, v157, v5
	ds_write_b16 v158, v2
	ds_write_b16_d16_hi v158, v2 offset:144
	v_cvt_pk_f16_f32 v2, v203, v204
	v_cvt_pk_f16_f32 v4, v1, v160
	v_add_f32_e32 v161, v157, v6
	v_add_f32_e32 v163, v157, v7
	v_add_f32_e32 v164, v157, v23
	ds_write_b16 v158, v2 offset:288
	ds_write_b16_d16_hi v158, v2 offset:4896
	ds_write_b16 v158, v4 offset:432
	ds_write_b16_d16_hi v158, v4 offset:5040
	v_cvt_pk_f16_f32 v2, v161, v162
	v_cvt_pk_f16_f32 v4, v163, v164
	v_add_f32_e32 v165, v157, v8
	v_add_f32_e32 v166, v157, v24
	v_add_f32_e32 v167, v157, v9
	v_add_f32_e32 v168, v157, v25
	ds_write_b16 v158, v2 offset:1152
	ds_write_b16_d16_hi v158, v2 offset:5760
	ds_write_b16 v158, v4 offset:1296
	ds_write_b16_d16_hi v158, v4 offset:5904
	v_cvt_pk_f16_f32 v2, v165, v166
	v_cvt_pk_f16_f32 v4, v167, v168
	v_add_f32_e32 v169, v157, v10
	v_add_f32_e32 v170, v157, v26
	v_add_f32_e32 v171, v157, v11
	v_add_f32_e32 v172, v157, v27
	ds_write_b16 v158, v2 offset:1440
	ds_write_b16_d16_hi v158, v2 offset:6048
	ds_write_b16 v158, v4 offset:1584
	ds_write_b16_d16_hi v158, v4 offset:6192
	v_cvt_pk_f16_f32 v2, v169, v170
	v_cvt_pk_f16_f32 v4, v171, v172
	v_add_f32_e32 v173, v157, v12
	v_add_f32_e32 v174, v157, v28
	v_add_f32_e32 v175, v157, v13
	v_add_f32_e32 v176, v157, v29
	ds_write_b16 v158, v2 offset:2304
	ds_write_b16_d16_hi v158, v2 offset:6912
	ds_write_b16 v158, v4 offset:2448
	ds_write_b16_d16_hi v158, v4 offset:7056
	v_cvt_pk_f16_f32 v2, v173, v174
	v_cvt_pk_f16_f32 v4, v175, v176
	v_add_f32_e32 v177, v157, v14
	v_add_f32_e32 v178, v157, v30
	v_add_f32_e32 v179, v157, v15
	v_add_f32_e32 v180, v157, v31
	ds_write_b16 v158, v2 offset:2592
	ds_write_b16_d16_hi v158, v2 offset:7200
	ds_write_b16 v158, v4 offset:2736
	ds_write_b16_d16_hi v158, v4 offset:7344
	v_cvt_pk_f16_f32 v2, v177, v178
	v_cvt_pk_f16_f32 v4, v179, v180
	v_add_f32_e32 v200, v157, v19
	v_add_f32_e32 v181, v157, v16
	v_add_f32_e32 v183, v157, v32
	v_add_f32_e32 v182, v157, v17
	v_add_f32_e32 v184, v157, v33
	v_cvt_pk_f16_f32 v18, v200, v181
	ds_write_b16 v158, v2 offset:3456
	ds_write_b16_d16_hi v158, v2 offset:8064
	ds_write_b16 v158, v4 offset:3600
	ds_write_b16_d16_hi v158, v4 offset:8208
	v_cvt_pk_f16_f32 v3, v183, v182
	v_cvt_f16_f32_e32 v5, v184
	ds_write_b16 v158, v18 offset:4752
	ds_write_b16_d16_hi v158, v18 offset:3744
	ds_write_b16 v158, v3 offset:8352
	ds_write_b16_d16_hi v158, v3 offset:3888
	ds_write_b16 v158, v5 offset:8496
	s_waitcnt lgkmcnt(0)
	s_barrier
	ds_read_b128 v[2:5], v159 offset:34816
	ds_read_b128 v[18:21], v159 offset:43520
	ds_read_b128 v[140:143], v159 offset:34848
	ds_read_b128 v[144:147], v159 offset:43552
	s_waitcnt lgkmcnt(3)
	v_mfma_f32_32x32x16_f16 v[50:65], v[2:5], v[126:129], 0
	s_add_u32 s0, s2, s0
	s_addc_u32 s1, s3, s1
	s_waitcnt lgkmcnt(2)
	v_mfma_f32_32x32x16_f16 v[34:49], v[18:21], v[126:129], 0
	v_mfma_f32_32x32x16_f16 v[2:17], v[2:5], v[122:125], 0
	v_mfma_f32_32x32x16_f16 v[18:33], v[18:21], v[122:125], 0
	ds_read_b128 v[242:245], v159 offset:34880
	ds_read_b128 v[246:249], v159 offset:43584
	s_waitcnt lgkmcnt(3)
	v_mfma_f32_32x32x16_f16 v[50:65], v[140:143], v[118:121], v[50:65]
	s_waitcnt lgkmcnt(2)
	v_mfma_f32_32x32x16_f16 v[34:49], v[144:147], v[118:121], v[34:49]
	v_mfma_f32_32x32x16_f16 v[2:17], v[140:143], v[114:117], v[2:17]
	v_mfma_f32_32x32x16_f16 v[18:33], v[144:147], v[114:117], v[18:33]
	ds_read_b128 v[140:143], v159 offset:34912
	ds_read_b128 v[144:147], v159 offset:43616
	s_waitcnt lgkmcnt(3)
	v_mfma_f32_32x32x16_f16 v[50:65], v[242:245], v[110:113], v[50:65]
	s_waitcnt lgkmcnt(2)
	v_mfma_f32_32x32x16_f16 v[34:49], v[246:249], v[110:113], v[34:49]
	v_mfma_f32_32x32x16_f16 v[2:17], v[242:245], v[106:109], v[2:17]
	v_mfma_f32_32x32x16_f16 v[18:33], v[246:249], v[106:109], v[18:33]
	ds_read_b128 v[242:245], v159 offset:34944
	ds_read_b128 v[246:249], v159 offset:43648
	s_waitcnt lgkmcnt(3)
	v_mfma_f32_32x32x16_f16 v[50:65], v[140:143], v[102:105], v[50:65]
	s_waitcnt lgkmcnt(2)
	v_mfma_f32_32x32x16_f16 v[34:49], v[144:147], v[102:105], v[34:49]
	v_mfma_f32_32x32x16_f16 v[2:17], v[140:143], v[98:101], v[2:17]
	v_mfma_f32_32x32x16_f16 v[18:33], v[144:147], v[98:101], v[18:33]
	ds_read_b128 v[186:189], v159 offset:34976
	ds_read_b128 v[206:209], v159 offset:43680
	s_waitcnt lgkmcnt(3)
	v_mfma_f32_32x32x16_f16 v[50:65], v[242:245], v[94:97], v[50:65]
	s_waitcnt lgkmcnt(2)
	v_mfma_f32_32x32x16_f16 v[34:49], v[246:249], v[94:97], v[34:49]
	v_mfma_f32_32x32x16_f16 v[2:17], v[242:245], v[86:89], v[2:17]
	v_mfma_f32_32x32x16_f16 v[18:33], v[246:249], v[86:89], v[18:33]
	ds_read_b128 v[140:143], v159 offset:35008
	ds_read_b128 v[144:147], v159 offset:43712
	s_waitcnt lgkmcnt(3)
	v_mfma_f32_32x32x16_f16 v[50:65], v[186:189], v[90:93], v[50:65]
	s_waitcnt lgkmcnt(2)
	v_mfma_f32_32x32x16_f16 v[34:49], v[206:209], v[90:93], v[34:49]
	v_mfma_f32_32x32x16_f16 v[2:17], v[186:189], v[78:81], v[2:17]
	v_mfma_f32_32x32x16_f16 v[18:33], v[206:209], v[78:81], v[18:33]
	ds_read_b128 v[186:189], v159 offset:35040
	ds_read_b128 v[206:209], v159 offset:43744
	s_waitcnt lgkmcnt(3)
	v_mfma_f32_32x32x16_f16 v[50:65], v[140:143], v[82:85], v[50:65]
	s_waitcnt lgkmcnt(2)
	v_mfma_f32_32x32x16_f16 v[34:49], v[144:147], v[82:85], v[34:49]
	v_mfma_f32_32x32x16_f16 v[2:17], v[140:143], v[70:73], v[2:17]
	v_lshlrev_b32_e32 v140, 3, v148
	v_and_b32_e32 v185, 0x1f8, v140
	global_load_dwordx2 v[148:149], v185, s[0:1]
	global_load_dwordx2 v[142:143], v185, s[0:1] offset:1024
	global_load_dwordx2 v[140:141], v185, s[0:1] offset:1536
	v_mfma_f32_32x32x16_f16 v[18:33], v[144:147], v[70:73], v[18:33]
	global_load_dwordx2 v[144:145], v185, s[0:1] offset:512
	global_load_dwordx2 v[146:147], v185, s[0:1] offset:2048
	s_waitcnt lgkmcnt(1)
	v_mfma_f32_32x32x16_f16 v[50:65], v[186:189], v[74:77], v[50:65]
	v_mfma_f32_32x32x16_f16 v[2:17], v[186:189], v[66:69], v[2:17]
	s_nop 10
	v_cvt_pk_f16_f32 v57, v56, v57
	v_cvt_pk_f16_f32 v56, v54, v55
	v_cvt_pk_f16_f32 v54, v50, v51
	s_waitcnt vmcnt(12)
	v_cvt_pk_f16_f32 v55, v52, v53
	s_waitcnt vmcnt(8)
	v_perm_b32 v50, v240, v138, s42
	v_perm_b32 v51, v240, v138, s43
	v_perm_b32 v52, v240, v139, s42
	v_perm_b32 v53, v240, v139, s43
	v_perm_b32 v139, v240, v136, s43
	v_pk_add_f16 v50, v50, s5 op_sel_hi:[1,0]
	v_pk_add_f16 v51, v51, s5 op_sel_hi:[1,0]
	v_pk_add_f16 v52, v52, s5 op_sel_hi:[1,0]
	v_pk_add_f16 v53, v53, s5 op_sel_hi:[1,0]
	v_perm_b32 v190, v240, v137, s42
	s_waitcnt lgkmcnt(0)
	v_mfma_f32_32x32x16_f16 v[18:33], v[206:209], v[66:69], v[18:33]
	v_perm_b32 v138, v240, v136, s42
	v_perm_b32 v191, v240, v137, s43
	v_pk_add_f16 v136, v138, s5 op_sel_hi:[1,0]
	v_pk_add_f16 v137, v139, s5 op_sel_hi:[1,0]
	v_pk_add_f16 v138, v190, s5 op_sel_hi:[1,0]
	v_pk_add_f16 v139, v191, s5 op_sel_hi:[1,0]
	v_cvt_pk_f16_f32 v65, v64, v65
	v_cvt_pk_f16_f32 v64, v62, v63
	v_cvt_pk_f16_f32 v63, v60, v61
	v_cvt_pk_f16_f32 v62, v58, v59
	v_mfma_f32_32x32x16_f16 v[34:49], v[206:209], v[74:77], v[34:49]
	v_mfma_f32_32x32x16_f16 v[2:17], v[50:53], v[54:57], v[2:17]
	s_waitcnt vmcnt(7)
	v_perm_b32 v58, v240, v134, s42
	v_perm_b32 v59, v240, v134, s43
	v_perm_b32 v60, v240, v135, s42
	v_perm_b32 v61, v240, v135, s43
	v_pk_add_f16 v58, v58, s5 op_sel_hi:[1,0]
	v_pk_add_f16 v59, v59, s5 op_sel_hi:[1,0]
	v_pk_add_f16 v60, v60, s5 op_sel_hi:[1,0]
	v_pk_add_f16 v61, v61, s5 op_sel_hi:[1,0]
	v_mfma_f32_32x32x16_f16 v[18:33], v[136:139], v[54:57], v[18:33]
	v_perm_b32 v134, v240, v154, s42
	v_perm_b32 v135, v240, v154, s43
	v_perm_b32 v154, v240, v155, s42
	v_perm_b32 v155, v240, v155, s43
	v_pk_add_f16 v210, v134, s5 op_sel_hi:[1,0]
	v_pk_add_f16 v211, v135, s5 op_sel_hi:[1,0]
	v_pk_add_f16 v212, v154, s5 op_sel_hi:[1,0]
	v_pk_add_f16 v213, v155, s5 op_sel_hi:[1,0]
	v_cvt_pk_f16_f32 v41, v40, v41
	v_cvt_pk_f16_f32 v40, v38, v39
	v_cvt_pk_f16_f32 v39, v36, v37
	v_cvt_pk_f16_f32 v38, v34, v35
	v_mfma_f32_32x32x16_f16 v[2:17], v[58:61], v[62:65], v[2:17]
	v_perm_b32 v34, v240, v132, s42
	v_perm_b32 v35, v240, v132, s43
	v_perm_b32 v36, v240, v133, s42
	v_perm_b32 v37, v240, v133, s43
	v_pk_add_f16 v34, v34, s5 op_sel_hi:[1,0]
	v_pk_add_f16 v35, v35, s5 op_sel_hi:[1,0]
	v_pk_add_f16 v36, v36, s5 op_sel_hi:[1,0]
	v_pk_add_f16 v37, v37, s5 op_sel_hi:[1,0]
	s_waitcnt vmcnt(6)
	v_mfma_f32_32x32x16_f16 v[18:33], v[210:213], v[62:65], v[18:33]
	v_perm_b32 v132, v240, v152, s42
	v_perm_b32 v133, v240, v152, s43
	v_perm_b32 v134, v240, v153, s42
	v_perm_b32 v53, v240, v153, s43
	v_pk_add_f16 v50, v132, s5 op_sel_hi:[1,0]
	v_pk_add_f16 v51, v133, s5 op_sel_hi:[1,0]
	v_pk_add_f16 v52, v134, s5 op_sel_hi:[1,0]
	v_pk_add_f16 v53, v53, s5 op_sel_hi:[1,0]
	v_cvt_pk_f16_f32 v49, v48, v49
	v_cvt_pk_f16_f32 v48, v46, v47
	v_cvt_pk_f16_f32 v47, v44, v45
	v_cvt_pk_f16_f32 v46, v42, v43
	v_mfma_f32_32x32x16_f16 v[2:17], v[34:37], v[38:41], v[2:17]
	v_perm_b32 v42, v240, v130, s42
	v_perm_b32 v43, v240, v130, s43
	v_perm_b32 v44, v240, v131, s42
	v_perm_b32 v45, v240, v131, s43
	v_pk_add_f16 v42, v42, s5 op_sel_hi:[1,0]
	v_pk_add_f16 v43, v43, s5 op_sel_hi:[1,0]
	v_pk_add_f16 v44, v44, s5 op_sel_hi:[1,0]
	v_pk_add_f16 v45, v45, s5 op_sel_hi:[1,0]
	s_waitcnt vmcnt(5)
	v_mfma_f32_32x32x16_f16 v[18:33], v[50:53], v[38:41], v[18:33]
	v_perm_b32 v34, v240, v150, s42
	v_perm_b32 v35, v240, v150, s43
	v_perm_b32 v36, v240, v151, s42
	v_perm_b32 v37, v240, v151, s43
	v_pk_add_f16 v34, v34, s5 op_sel_hi:[1,0]
	v_pk_add_f16 v35, v35, s5 op_sel_hi:[1,0]
	v_pk_add_f16 v36, v36, s5 op_sel_hi:[1,0]
	v_pk_add_f16 v37, v37, s5 op_sel_hi:[1,0]
	v_mfma_f32_32x32x16_f16 v[2:17], v[42:45], v[46:49], v[2:17]
	global_load_dwordx2 v[154:155], v185, s[0:1] offset:2560
	global_load_dwordx2 v[152:153], v185, s[0:1] offset:3072
	global_load_dwordx2 v[150:151], v185, s[0:1] offset:3584
	s_or_b32 s0, s8, 6
	s_ashr_i32 s1, s0, 31
	s_lshl_b64 s[0:1], s[0:1], 12
	s_add_u32 s0, s2, s0
	v_mfma_f32_32x32x16_f16 v[18:33], v[34:37], v[46:49], v[18:33]
	s_nop 3
	v_add_f32_e32 v185, v157, v2
	v_add_f32_e32 v187, v157, v3
	v_cvt_pk_f16_f32 v2, v185, v187
	v_add_f32_e32 v189, v157, v4
	v_add_f32_e32 v191, v157, v5
	ds_write_b16 v158, v2 offset:18432
	s_nop 0
	s_nop 0
	v_add_f32_e32 v190, v157, v20
	v_add_f32_e32 v192, v157, v21
	ds_write_b16_d16_hi v158, v2 offset:18576
	v_cvt_pk_f16_f32 v2, v189, v190
	v_cvt_pk_f16_f32 v4, v191, v192
	v_add_f32_e32 v194, v157, v6
	v_add_f32_e32 v195, v157, v22
	v_add_f32_e32 v197, v157, v7
	v_add_f32_e32 v199, v157, v23
	ds_write_b16 v158, v2 offset:18720
	ds_write_b16_d16_hi v158, v2 offset:23328
	ds_write_b16 v158, v4 offset:18864
	ds_write_b16_d16_hi v158, v4 offset:23472
	v_cvt_pk_f16_f32 v2, v194, v195
	v_cvt_pk_f16_f32 v4, v197, v199
	v_add_f32_e32 v201, v157, v8
	v_add_f32_e32 v202, v157, v24
	v_add_f32_e32 v205, v157, v9
	v_add_f32_e32 v206, v157, v25
	ds_write_b16 v158, v2 offset:19584
	ds_write_b16_d16_hi v158, v2 offset:24192
	ds_write_b16 v158, v4 offset:19728
	ds_write_b16_d16_hi v158, v4 offset:24336
	v_cvt_pk_f16_f32 v2, v201, v202
	v_cvt_pk_f16_f32 v4, v205, v206
	v_add_f32_e32 v207, v157, v10
	v_add_f32_e32 v209, v157, v26
	v_add_f32_e32 v208, v157, v11
	v_add_f32_e32 v210, v157, v27
	ds_write_b16 v158, v2 offset:19872
	ds_write_b16_d16_hi v158, v2 offset:24480
	ds_write_b16 v158, v4 offset:20016
	ds_write_b16_d16_hi v158, v4 offset:24624
	v_cvt_pk_f16_f32 v2, v207, v209
	v_cvt_pk_f16_f32 v4, v208, v210
	v_add_f32_e32 v211, v157, v12
	v_add_f32_e32 v212, v157, v28
	v_add_f32_e32 v213, v157, v13
	v_add_f32_e32 v214, v157, v29
	ds_write_b16 v158, v2 offset:20736
	ds_write_b16_d16_hi v158, v2 offset:25344
	ds_write_b16 v158, v4 offset:20880
	ds_write_b16_d16_hi v158, v4 offset:25488
	v_cvt_pk_f16_f32 v2, v211, v212
	v_cvt_pk_f16_f32 v4, v213, v214
	v_add_f32_e32 v215, v157, v14
	v_add_f32_e32 v216, v157, v30
	v_add_f32_e32 v217, v157, v15
	v_add_f32_e32 v218, v157, v31
	ds_write_b16 v158, v2 offset:21024
	ds_write_b16_d16_hi v158, v2 offset:25632
	ds_write_b16 v158, v4 offset:21168
	ds_write_b16_d16_hi v158, v4 offset:25776
	v_cvt_pk_f16_f32 v2, v215, v216
	v_cvt_pk_f16_f32 v4, v217, v218
	v_add_f32_e32 v186, v157, v18
	v_add_f32_e32 v188, v157, v19
	v_add_f32_e32 v219, v157, v16
	v_add_f32_e32 v221, v157, v32
	v_add_f32_e32 v220, v157, v17
	v_add_f32_e32 v222, v157, v33
	v_cvt_pk_f16_f32 v18, v186, v188
	ds_write_b16 v158, v2 offset:21888
	ds_write_b16_d16_hi v158, v2 offset:26496
	ds_write_b16 v158, v4 offset:22032
	ds_write_b16_d16_hi v158, v4 offset:26640
	v_cvt_pk_f16_f32 v2, v219, v221
	v_cvt_pk_f16_f32 v4, v220, v222
	ds_write_b16 v158, v18 offset:23040
	ds_write_b16_d16_hi v158, v18 offset:23184
	ds_write_b16 v158, v2 offset:22176
	ds_write_b16_d16_hi v158, v2 offset:26784
	ds_write_b16 v158, v4 offset:22320
	ds_write_b16_d16_hi v158, v4 offset:26928
	s_waitcnt lgkmcnt(0)
	s_barrier
	ds_read_b128 v[2:5], v159
	ds_read_b128 v[18:21], v159 offset:8704
	s_waitcnt lgkmcnt(1)
	v_mfma_f32_32x32x16_f16 v[50:65], v[2:5], v[126:129], 0
	v_lshlrev_b32_e32 v0, 3, v0
	s_addc_u32 s1, s3, s1
	v_and_b32_e32 v0, 0x1f8, v0
	global_load_dwordx2 v[138:139], v0, s[0:1]
	s_waitcnt lgkmcnt(0)
	v_mfma_f32_32x32x16_f16 v[34:49], v[18:21], v[126:129], 0
	v_mfma_f32_32x32x16_f16 v[2:17], v[2:5], v[122:125], 0
	v_mfma_f32_32x32x16_f16 v[18:33], v[18:21], v[122:125], 0
	ds_read_b128 v[130:133], v159 offset:32
	ds_read_b128 v[134:137], v159 offset:8736
	s_waitcnt lgkmcnt(1)
	v_mfma_f32_32x32x16_f16 v[50:65], v[130:133], v[118:121], v[50:65]
	s_waitcnt lgkmcnt(0)
	v_mfma_f32_32x32x16_f16 v[34:49], v[134:137], v[118:121], v[34:49]
	v_mfma_f32_32x32x16_f16 v[2:17], v[130:133], v[114:117], v[2:17]
	v_mfma_f32_32x32x16_f16 v[18:33], v[134:137], v[114:117], v[18:33]
	ds_read_b128 v[224:227], v159 offset:64
	ds_read_b128 v[228:231], v159 offset:8768
	ds_read_b128 v[130:133], v159 offset:96
	ds_read_b128 v[134:137], v159 offset:8800
	s_waitcnt lgkmcnt(3)
	v_mfma_f32_32x32x16_f16 v[50:65], v[224:227], v[110:113], v[50:65]
	s_waitcnt lgkmcnt(2)
	v_mfma_f32_32x32x16_f16 v[34:49], v[228:231], v[110:113], v[34:49]
	v_mfma_f32_32x32x16_f16 v[2:17], v[224:227], v[106:109], v[2:17]
	v_mfma_f32_32x32x16_f16 v[18:33], v[228:231], v[106:109], v[18:33]
	ds_read_b128 v[224:227], v159 offset:128
	ds_read_b128 v[228:231], v159 offset:8832
	s_waitcnt lgkmcnt(3)
	v_mfma_f32_32x32x16_f16 v[50:65], v[130:133], v[102:105], v[50:65]
	s_waitcnt lgkmcnt(2)
	v_mfma_f32_32x32x16_f16 v[34:49], v[134:137], v[102:105], v[34:49]
	v_mfma_f32_32x32x16_f16 v[2:17], v[130:133], v[98:101], v[2:17]
	v_mfma_f32_32x32x16_f16 v[18:33], v[134:137], v[98:101], v[18:33]
	ds_read_b128 v[130:133], v159 offset:160
	ds_read_b128 v[134:137], v159 offset:8864
	s_waitcnt lgkmcnt(3)
	v_mfma_f32_32x32x16_f16 v[50:65], v[224:227], v[94:97], v[50:65]
	s_waitcnt lgkmcnt(2)
	v_mfma_f32_32x32x16_f16 v[34:49], v[228:231], v[94:97], v[34:49]
	v_mfma_f32_32x32x16_f16 v[2:17], v[224:227], v[86:89], v[2:17]
	v_mfma_f32_32x32x16_f16 v[18:33], v[228:231], v[86:89], v[18:33]
	ds_read_b128 v[224:227], v159 offset:192
	ds_read_b128 v[228:231], v159 offset:8896
	s_waitcnt lgkmcnt(3)
	v_mfma_f32_32x32x16_f16 v[50:65], v[130:133], v[90:93], v[50:65]
	s_waitcnt lgkmcnt(2)
	v_mfma_f32_32x32x16_f16 v[34:49], v[134:137], v[90:93], v[34:49]
	v_mfma_f32_32x32x16_f16 v[2:17], v[130:133], v[78:81], v[2:17]
	v_add_f32_e32 v130, v193, v196
	v_add_f32_e32 v130, 0, v130
	v_add_f32_e32 v132, v198, v200
	v_add_f32_e32 v130, v132, v130
	v_mul_f32_e32 v132, v200, v200
	v_fmac_f32_e32 v132, v198, v198
	v_mul_f32_e32 v131, v196, v196
	v_mfma_f32_32x32x16_f16 v[18:33], v[134:137], v[78:81], v[18:33]
	ds_read_b128 v[232:235], v159 offset:224
	ds_read_b128 v[236:239], v159 offset:8928
	v_fmac_f32_e32 v131, v193, v193
	v_add_f32_e32 v131, v131, v132
	v_add_f32_e32 v132, v203, v204
	v_add_f32_e32 v130, v132, v130
	v_mul_f32_e32 v132, v204, v204
	s_waitcnt lgkmcnt(3)
	v_mfma_f32_32x32x16_f16 v[50:65], v[224:227], v[82:85], v[50:65]
	v_fmac_f32_e32 v132, v203, v203
	v_add_f32_e32 v193, v132, v131
	v_add_f32_e32 v131, v1, v160
	v_add_f32_e32 v196, v131, v130
	global_load_dwordx2 v[134:135], v0, s[0:1] offset:512
	global_load_dwordx2 v[132:133], v0, s[0:1] offset:1024
	global_load_dwordx2 v[130:131], v0, s[0:1] offset:1536
	s_waitcnt lgkmcnt(2)
	v_mfma_f32_32x32x16_f16 v[34:49], v[228:231], v[82:85], v[34:49]
	global_load_dwordx2 v[136:137], v0, s[0:1] offset:2048
	v_mfma_f32_32x32x16_f16 v[2:17], v[224:227], v[70:73], v[2:17]
	v_mfma_f32_32x32x16_f16 v[18:33], v[228:231], v[70:73], v[18:33]
	s_waitcnt lgkmcnt(1)
	v_mfma_f32_32x32x16_f16 v[50:65], v[232:235], v[74:77], v[50:65]
	v_mfma_f32_32x32x16_f16 v[2:17], v[232:235], v[66:69], v[2:17]
	s_nop 10
	v_cvt_pk_f16_f32 v57, v56, v57
	v_cvt_pk_f16_f32 v56, v54, v55
	v_cvt_pk_f16_f32 v54, v50, v51
	s_waitcnt vmcnt(12)
	v_lshlrev_b32_e32 v50, 8, v148
	v_cvt_pk_f16_f32 v55, v52, v53
	v_perm_b32 v50, v50, v148, s4
	v_lshrrev_b32_e32 v51, 16, v148
	v_lshrrev_b32_e32 v52, 8, v148
	v_lshrrev_b32_e32 v53, 16, v149
	v_lshrrev_b32_e32 v148, 8, v149
	v_perm_b32 v51, v52, v51, s4
	v_lshlrev_b32_e32 v52, 8, v149
	v_perm_b32 v53, v148, v53, s4
	s_waitcnt vmcnt(8)
	v_perm_b32 v52, v52, v149, s4
	v_perm_b32 v149, v240, v146, s43
	v_perm_b32 v198, v240, v147, s42
	s_waitcnt lgkmcnt(0)
	v_mfma_f32_32x32x16_f16 v[18:33], v[236:239], v[66:69], v[18:33]
	v_or_b32_e32 v50, 0x64006400, v50
	v_or_b32_e32 v51, 0x64006400, v51
	v_or_b32_e32 v52, 0x64006400, v52
	v_or_b32_e32 v53, 0x64006400, v53
	v_pk_add_f16 v50, v50, s5 op_sel_hi:[1,0]
	v_pk_add_f16 v51, v51, s5 op_sel_hi:[1,0]
	v_pk_add_f16 v52, v52, s5 op_sel_hi:[1,0]
	v_pk_add_f16 v53, v53, s5 op_sel_hi:[1,0]
	v_perm_b32 v148, v240, v146, s42
	v_perm_b32 v200, v240, v147, s43
	v_pk_add_f16 v146, v148, s5 op_sel_hi:[1,0]
	v_pk_add_f16 v147, v149, s5 op_sel_hi:[1,0]
	v_pk_add_f16 v148, v198, s5 op_sel_hi:[1,0]
	v_pk_add_f16 v149, v200, s5 op_sel_hi:[1,0]
	v_cvt_pk_f16_f32 v65, v64, v65
	v_cvt_pk_f16_f32 v64, v62, v63
	v_cvt_pk_f16_f32 v62, v58, v59
	v_cvt_pk_f16_f32 v63, v60, v61
	s_waitcnt vmcnt(7)
	v_mfma_f32_32x32x16_f16 v[34:49], v[236:239], v[74:77], v[34:49]
	v_mfma_f32_32x32x16_f16 v[2:17], v[50:53], v[54:57], v[2:17]
	v_perm_b32 v58, v240, v144, s42
	v_perm_b32 v59, v240, v144, s43
	v_perm_b32 v60, v240, v145, s42
	v_perm_b32 v61, v240, v145, s43
	v_mfma_f32_32x32x16_f16 v[18:33], v[146:149], v[54:57], v[18:33]
	v_pk_add_f16 v58, v58, s5 op_sel_hi:[1,0]
	v_pk_add_f16 v59, v59, s5 op_sel_hi:[1,0]
	v_pk_add_f16 v60, v60, s5 op_sel_hi:[1,0]
	v_pk_add_f16 v61, v61, s5 op_sel_hi:[1,0]
	v_perm_b32 v144, v240, v154, s42
	v_perm_b32 v145, v240, v154, s43
	v_perm_b32 v154, v240, v155, s42
	v_perm_b32 v155, v240, v155, s43
	v_pk_add_f16 v224, v144, s5 op_sel_hi:[1,0]
	v_pk_add_f16 v225, v145, s5 op_sel_hi:[1,0]
	v_pk_add_f16 v226, v154, s5 op_sel_hi:[1,0]
	v_pk_add_f16 v227, v155, s5 op_sel_hi:[1,0]
	v_cvt_pk_f16_f32 v41, v40, v41
	v_cvt_pk_f16_f32 v40, v38, v39
	v_cvt_pk_f16_f32 v39, v36, v37
	v_cvt_pk_f16_f32 v38, v34, v35
	s_waitcnt vmcnt(6)
	v_mfma_f32_32x32x16_f16 v[2:17], v[58:61], v[62:65], v[2:17]
	v_perm_b32 v34, v240, v142, s42
	v_perm_b32 v35, v240, v142, s43
	v_mfma_f32_32x32x16_f16 v[18:33], v[224:227], v[62:65], v[18:33]
	v_perm_b32 v36, v240, v143, s42
	v_perm_b32 v37, v240, v143, s43
	v_pk_add_f16 v34, v34, s5 op_sel_hi:[1,0]
	v_pk_add_f16 v35, v35, s5 op_sel_hi:[1,0]
	v_pk_add_f16 v36, v36, s5 op_sel_hi:[1,0]
	v_pk_add_f16 v37, v37, s5 op_sel_hi:[1,0]
	v_perm_b32 v142, v240, v152, s42
	v_perm_b32 v143, v240, v152, s43
	v_perm_b32 v144, v240, v153, s42
	v_perm_b32 v53, v240, v153, s43
	v_pk_add_f16 v50, v142, s5 op_sel_hi:[1,0]
	v_pk_add_f16 v51, v143, s5 op_sel_hi:[1,0]
	v_pk_add_f16 v52, v144, s5 op_sel_hi:[1,0]
	v_pk_add_f16 v53, v53, s5 op_sel_hi:[1,0]
	v_cvt_pk_f16_f32 v49, v48, v49
	v_cvt_pk_f16_f32 v48, v46, v47
	v_cvt_pk_f16_f32 v47, v44, v45
	v_cvt_pk_f16_f32 v46, v42, v43
	v_mfma_f32_32x32x16_f16 v[2:17], v[34:37], v[38:41], v[2:17]
	s_waitcnt vmcnt(5)
	v_mfma_f32_32x32x16_f16 v[18:33], v[50:53], v[38:41], v[18:33]
	v_perm_b32 v42, v240, v140, s42
	v_perm_b32 v43, v240, v140, s43
	v_perm_b32 v44, v240, v141, s42
	v_perm_b32 v45, v240, v141, s43
	v_perm_b32 v34, v240, v150, s42
	v_perm_b32 v35, v240, v150, s43
	v_perm_b32 v36, v240, v151, s42
	v_perm_b32 v37, v240, v151, s43
	v_pk_add_f16 v42, v42, s5 op_sel_hi:[1,0]
	v_pk_add_f16 v43, v43, s5 op_sel_hi:[1,0]
	v_pk_add_f16 v44, v44, s5 op_sel_hi:[1,0]
	v_pk_add_f16 v45, v45, s5 op_sel_hi:[1,0]
	v_pk_add_f16 v34, v34, s5 op_sel_hi:[1,0]
	v_pk_add_f16 v35, v35, s5 op_sel_hi:[1,0]
	v_pk_add_f16 v36, v36, s5 op_sel_hi:[1,0]
	v_pk_add_f16 v37, v37, s5 op_sel_hi:[1,0]
	v_mfma_f32_32x32x16_f16 v[2:17], v[42:45], v[46:49], v[2:17]
	global_load_dwordx2 v[142:143], v0, s[0:1] offset:2560
	global_load_dwordx2 v[140:141], v0, s[0:1] offset:3072
	global_load_dwordx2 v[64:65], v0, s[0:1] offset:3584
	v_mfma_f32_32x32x16_f16 v[18:33], v[34:37], v[46:49], v[18:33]
	s_nop 7
	v_add_f32_e32 v146, v157, v2
	v_add_f32_e32 v148, v157, v3
	v_cvt_pk_f16_f32 v0, v146, v148
	v_add_f32_e32 v150, v157, v4
	v_add_f32_e32 v152, v157, v5
	ds_write_b16 v158, v0
	v_add_f32_e32 v147, v157, v18
	v_cvt_f16_f32_e32 v2, v147
	v_add_f32_e32 v151, v157, v20
	v_add_f32_e32 v153, v157, v21
	ds_write_b16_d16_hi v158, v0 offset:144
	ds_write_b16 v158, v2 offset:4608
	v_cvt_pk_f16_f32 v0, v150, v151
	v_cvt_pk_f16_f32 v3, v152, v153
	v_add_f32_e32 v154, v157, v6
	v_add_f32_e32 v155, v157, v22
	v_add_f32_e32 v198, v157, v7
	v_add_f32_e32 v200, v157, v23
	ds_write_b16 v158, v0 offset:288
	ds_write_b16_d16_hi v158, v0 offset:4896
	ds_write_b16 v158, v3 offset:432
	ds_write_b16_d16_hi v158, v3 offset:5040
	v_cvt_pk_f16_f32 v0, v154, v155
	v_cvt_pk_f16_f32 v3, v198, v200
	v_add_f32_e32 v203, v157, v8
	v_add_f32_e32 v204, v157, v24
	v_add_f32_e32 v223, v157, v9
	v_add_f32_e32 v224, v157, v25
	ds_write_b16 v158, v0 offset:1152
	ds_write_b16_d16_hi v158, v0 offset:5760
	ds_write_b16 v158, v3 offset:1296
	ds_write_b16_d16_hi v158, v3 offset:5904
	v_cvt_pk_f16_f32 v0, v203, v204
	v_cvt_pk_f16_f32 v3, v223, v224
	v_add_f32_e32 v225, v157, v10
	v_add_f32_e32 v226, v157, v26
	v_add_f32_e32 v227, v157, v11
	v_add_f32_e32 v228, v157, v27
	ds_write_b16 v158, v0 offset:1440
	ds_write_b16_d16_hi v158, v0 offset:6048
	ds_write_b16 v158, v3 offset:1584
	ds_write_b16_d16_hi v158, v3 offset:6192
	v_cvt_pk_f16_f32 v0, v225, v226
	v_cvt_pk_f16_f32 v3, v227, v228
	v_add_f32_e32 v229, v157, v12
	v_add_f32_e32 v230, v157, v28
	v_add_f32_e32 v231, v157, v13
	v_add_f32_e32 v232, v157, v29
	ds_write_b16 v158, v0 offset:2304
	ds_write_b16_d16_hi v158, v0 offset:6912
	ds_write_b16 v158, v3 offset:2448
	ds_write_b16_d16_hi v158, v3 offset:7056
	v_cvt_pk_f16_f32 v0, v229, v230
	v_cvt_pk_f16_f32 v3, v231, v232
	v_add_f32_e32 v233, v157, v14
	v_add_f32_e32 v234, v157, v30
	v_add_f32_e32 v235, v157, v15
	v_add_f32_e32 v236, v157, v31
	ds_write_b16 v158, v0 offset:2592
	ds_write_b16_d16_hi v158, v0 offset:7200
	ds_write_b16 v158, v3 offset:2736
	ds_write_b16_d16_hi v158, v3 offset:7344
	v_cvt_pk_f16_f32 v0, v233, v234
	v_cvt_pk_f16_f32 v3, v235, v236
	v_add_f32_e32 v149, v157, v19
	v_add_f32_e32 v237, v157, v16
	v_add_f32_e32 v238, v157, v32
	v_add_f32_e32 v144, v157, v17
	v_add_f32_e32 v145, v157, v33
	v_cvt_pk_f16_f32 v18, v149, v237
	ds_write_b16 v158, v0 offset:3456
	ds_write_b16_d16_hi v158, v0 offset:8064
	ds_write_b16 v158, v3 offset:3600
	ds_write_b16_d16_hi v158, v3 offset:8208
	v_cvt_pk_f16_f32 v2, v238, v144
	v_cvt_f16_f32_e32 v4, v145
	ds_write_b16 v158, v18 offset:4752
	ds_write_b16_d16_hi v158, v18 offset:3744
	ds_write_b16 v158, v2 offset:8352
	ds_write_b16_d16_hi v158, v2 offset:3888
	ds_write_b16 v158, v4 offset:8496
	s_waitcnt lgkmcnt(0)
	s_barrier
	ds_read_b128 v[16:19], v159 offset:43520
	s_waitcnt lgkmcnt(0)
	v_mfma_f32_32x32x16_f16 v[32:47], v[16:19], v[126:129], 0
	ds_read_b128 v[2:5], v159 offset:34816
	v_mul_f32_e32 v0, v160, v160
	v_fmac_f32_e32 v0, v1, v1
	v_mul_f32_e32 v6, v162, v162
	v_add_f32_e32 v0, v0, v193
	v_add_f32_e32 v1, v161, v162
	v_fmac_f32_e32 v6, v161, v161
	s_waitcnt lgkmcnt(0)
	v_mfma_f32_32x32x16_f16 v[48:63], v[2:5], v[126:129], 0
	ds_read_b128 v[126:129], v159 offset:34848
	v_add_f32_e32 v1, v1, v196
	v_add_f32_e32 v0, v6, v0
	v_add_f32_e32 v6, v163, v164
	v_add_f32_e32 v1, v6, v1
	v_mul_f32_e32 v6, v164, v164
	v_fmac_f32_e32 v6, v163, v163
	v_add_f32_e32 v0, v6, v0
	v_add_f32_e32 v6, v165, v166
	v_add_f32_e32 v1, v6, v1
	v_mul_f32_e32 v6, v166, v166
	v_fmac_f32_e32 v6, v165, v165
	v_add_f32_e32 v20, v6, v0
	v_add_f32_e32 v0, v167, v168
	v_add_f32_e32 v21, v0, v1
	s_waitcnt lgkmcnt(0)
	v_mfma_f32_32x32x16_f16 v[48:63], v[126:129], v[118:121], v[48:63]
	v_mul_f32_e32 v22, v168, v168
	v_fmac_f32_e32 v22, v167, v167
	v_add_f32_e32 v160, v22, v20
	v_add_f32_e32 v20, v169, v170
	v_mul_f32_e32 v162, v170, v170
	v_add_f32_e32 v161, v20, v21
	v_fmac_f32_e32 v162, v169, v169
	v_mfma_f32_32x32x16_f16 v[0:15], v[2:5], v[122:125], 0
	v_mfma_f32_32x32x16_f16 v[0:15], v[126:129], v[114:117], v[0:15]
	v_mfma_f32_32x32x16_f16 v[16:31], v[16:19], v[122:125], 0
	v_add_f32_e32 v123, v171, v172
	v_add_f32_e32 v122, v162, v160
	v_add_f32_e32 v160, v123, v161
	v_mul_f32_e32 v123, v172, v172
	v_fmac_f32_e32 v123, v171, v171
	v_add_f32_e32 v161, v123, v122
	ds_read_b128 v[122:125], v159 offset:43552
	v_add_f32_e32 v162, v173, v174
	v_add_f32_e32 v160, v162, v160
	v_mul_f32_e32 v162, v174, v174
	v_fmac_f32_e32 v162, v173, v173
	s_waitcnt lgkmcnt(0)
	v_mfma_f32_32x32x16_f16 v[32:47], v[122:125], v[118:121], v[32:47]
	v_mul_f32_e32 v118, v176, v176
	v_add_f32_e32 v161, v162, v161
	v_add_f32_e32 v162, v175, v176
	v_fmac_f32_e32 v118, v175, v175
	v_mul_f32_e32 v120, v178, v178
	v_add_f32_e32 v160, v162, v160
	v_add_f32_e32 v118, v118, v161
	v_add_f32_e32 v119, v177, v178
	v_fmac_f32_e32 v120, v177, v177
	v_add_f32_e32 v119, v119, v160
	v_add_f32_e32 v118, v120, v118
	v_add_f32_e32 v120, v179, v180
	v_add_f32_e32 v126, v120, v119
	v_mul_f32_e32 v119, v180, v180
	v_mfma_f32_32x32x16_f16 v[16:31], v[122:125], v[114:117], v[16:31]
	v_add_f32_e32 v114, v181, v183
	v_fmac_f32_e32 v119, v179, v179
	v_add_f32_e32 v122, v114, v126
	v_mul_f32_e32 v114, v183, v183
	v_add_f32_e32 v127, v119, v118
	v_fmac_f32_e32 v114, v181, v181
	ds_read_b128 v[118:121], v159 offset:34880
	v_add_f32_e32 v123, v114, v127
	ds_read_b128 v[114:117], v159 offset:43584
	v_add_f32_e32 v124, v182, v184
	v_add_f32_e32 v122, v124, v122
	v_mul_f32_e32 v124, v184, v184
	v_fmac_f32_e32 v124, v182, v182
	s_waitcnt lgkmcnt(1)
	v_mfma_f32_32x32x16_f16 v[48:63], v[118:121], v[110:113], v[48:63]
	v_add_f32_e32 v123, v124, v123
	v_add_f32_e32 v124, v185, v186
	v_add_f32_e32 v124, 0, v124
	v_add_f32_e32 v122, 0, v122
	s_waitcnt lgkmcnt(0)
	v_mfma_f32_32x32x16_f16 v[32:47], v[114:117], v[110:113], v[32:47]
	v_mul_f32_e32 v110, v186, v186
	v_mul_f32_e32 v112, v188, v188
	v_fmac_f32_e32 v110, v185, v185
	v_add_f32_e32 v111, v187, v188
	v_fmac_f32_e32 v112, v187, v187
	v_add_f32_e32 v111, v111, v124
	v_add_f32_e32 v110, v110, v112
	v_add_f32_e32 v112, v189, v190
	v_mfma_f32_32x32x16_f16 v[0:15], v[118:121], v[106:109], v[0:15]
	v_add_f32_e32 v118, v112, v111
	v_mul_f32_e32 v111, v190, v190
	v_fmac_f32_e32 v111, v189, v189
	v_add_f32_e32 v119, v111, v110
	v_add_f32_e32 v120, v191, v192
	ds_read_b128 v[110:113], v159 offset:34912
	v_mfma_f32_32x32x16_f16 v[16:31], v[114:117], v[106:109], v[16:31]
	v_mul_f32_e32 v107, v192, v192
	v_fmac_f32_e32 v107, v191, v191
	v_add_f32_e32 v106, v120, v118
	v_add_f32_e32 v114, v107, v119
	v_add_f32_e32 v107, v194, v195
	v_add_f32_e32 v115, v107, v106
	ds_read_b128 v[106:109], v159 offset:43616
	v_mul_f32_e32 v116, v195, v195
	v_fmac_f32_e32 v116, v194, v194
	v_add_f32_e32 v114, v116, v114
	v_add_f32_e32 v116, v197, v199
	v_add_f32_e32 v115, v116, v115
	v_mul_f32_e32 v116, v199, v199
	s_waitcnt lgkmcnt(1)
	v_mfma_f32_32x32x16_f16 v[48:63], v[110:113], v[102:105], v[48:63]
	v_fmac_f32_e32 v116, v197, v197
	s_waitcnt lgkmcnt(0)
	v_mfma_f32_32x32x16_f16 v[32:47], v[106:109], v[102:105], v[32:47]
	v_mul_f32_e32 v104, v202, v202
	v_add_f32_e32 v102, v116, v114
	v_add_f32_e32 v103, v201, v202
	v_fmac_f32_e32 v104, v201, v201
	v_add_f32_e32 v103, v103, v115
	v_add_f32_e32 v102, v104, v102
	v_add_f32_e32 v104, v205, v206
	v_add_f32_e32 v103, v104, v103
	v_mul_f32_e32 v104, v206, v206
	v_mfma_f32_32x32x16_f16 v[0:15], v[110:113], v[98:101], v[0:15]
	v_fmac_f32_e32 v104, v205, v205
	v_add_f32_e32 v110, v104, v102
	v_add_f32_e32 v102, v207, v209
	v_add_f32_e32 v111, v102, v103
	ds_read_b128 v[102:105], v159 offset:34944
	v_mfma_f32_32x32x16_f16 v[16:31], v[106:109], v[98:101], v[16:31]
	v_mul_f32_e32 v98, v209, v209
	v_fmac_f32_e32 v98, v207, v207
	v_add_f32_e32 v106, v98, v110
	v_add_f32_e32 v98, v208, v210
	v_add_f32_e32 v107, v98, v111
	ds_read_b128 v[98:101], v159 offset:43648
	v_mul_f32_e32 v108, v210, v210
	v_fmac_f32_e32 v108, v208, v208
	v_add_f32_e32 v106, v108, v106
	v_add_f32_e32 v108, v211, v212
	s_waitcnt lgkmcnt(1)
	v_mfma_f32_32x32x16_f16 v[48:63], v[102:105], v[94:97], v[48:63]
	v_add_f32_e32 v107, v108, v107
	v_mul_f32_e32 v108, v212, v212
	v_fmac_f32_e32 v108, v211, v211
	v_add_f32_e32 v106, v108, v106
	s_waitcnt lgkmcnt(0)
	v_mfma_f32_32x32x16_f16 v[32:47], v[98:101], v[94:97], v[32:47]
	v_add_f32_e32 v94, v213, v214
	v_add_f32_e32 v94, v94, v107
	v_mul_f32_e32 v95, v214, v214
	v_add_f32_e32 v96, v215, v216
	v_fmac_f32_e32 v95, v213, v213
	v_add_f32_e32 v94, v96, v94
	v_mul_f32_e32 v96, v216, v216
	v_add_f32_e32 v95, v95, v106
	v_fmac_f32_e32 v96, v215, v215
	v_mfma_f32_32x32x16_f16 v[0:15], v[102:105], v[86:89], v[0:15]
	v_add_f32_e32 v102, v96, v95
	v_add_f32_e32 v95, v217, v218
	v_add_f32_e32 v103, v95, v94
	ds_read_b128 v[94:97], v159 offset:34976
	v_mul_f32_e32 v104, v218, v218
	v_fmac_f32_e32 v104, v217, v217
	v_mfma_f32_32x32x16_f16 v[16:31], v[98:101], v[86:89], v[16:31]
	v_add_f32_e32 v86, v219, v221
	v_add_f32_e32 v99, v86, v103
	ds_read_b128 v[86:89], v159 offset:43680
	v_mul_f32_e32 v100, v221, v221
	v_add_f32_e32 v98, v104, v102
	v_fmac_f32_e32 v100, v219, v219
	v_add_f32_e32 v98, v100, v98
	s_waitcnt lgkmcnt(1)
	v_mfma_f32_32x32x16_f16 v[48:63], v[94:97], v[90:93], v[48:63]
	v_add_f32_e32 v100, v220, v222
	v_add_f32_e32 v99, v100, v99
	v_mul_f32_e32 v100, v222, v222
	v_fmac_f32_e32 v100, v220, v220
	v_add_f32_e32 v98, v100, v98
	v_add_f32_e32 v98, v123, v98
	v_add_f32_e32 v99, v122, v99
	s_waitcnt lgkmcnt(0)
	v_mfma_f32_32x32x16_f16 v[32:47], v[86:89], v[90:93], v[32:47]
	v_add_f32_e32 v90, v146, v147
	v_add_f32_e32 v90, 0, v90
	v_add_f32_e32 v92, v148, v149
	v_mul_f32_e32 v91, v147, v147
	v_add_f32_e32 v90, v92, v90
	v_mul_f32_e32 v92, v149, v149
	v_fmac_f32_e32 v91, v146, v146
	v_fmac_f32_e32 v92, v148, v148
	v_mfma_f32_32x32x16_f16 v[0:15], v[94:97], v[78:81], v[0:15]
	v_add_f32_e32 v94, v91, v92
	v_add_f32_e32 v91, v150, v151
	v_add_f32_e32 v95, v91, v90
	ds_read_b128 v[90:93], v159 offset:35008
	v_mul_f32_e32 v96, v151, v151
	v_fmac_f32_e32 v96, v150, v150
	v_mfma_f32_32x32x16_f16 v[16:31], v[86:89], v[78:81], v[16:31]
	v_add_f32_e32 v78, v152, v153
	v_add_f32_e32 v87, v78, v95
	ds_read_b128 v[78:81], v159 offset:43712
	v_mul_f32_e32 v88, v153, v153
	v_add_f32_e32 v86, v96, v94
	v_fmac_f32_e32 v88, v152, v152
	v_add_f32_e32 v86, v88, v86
	v_add_f32_e32 v88, v154, v155
	v_add_f32_e32 v87, v88, v87
	v_mul_f32_e32 v88, v155, v155
	v_fmac_f32_e32 v88, v154, v154
	v_add_f32_e32 v86, v88, v86
	v_add_f32_e32 v88, v198, v200
	s_waitcnt lgkmcnt(1)
	v_mfma_f32_32x32x16_f16 v[48:63], v[90:93], v[82:85], v[48:63]
	s_waitcnt lgkmcnt(0)
	v_mfma_f32_32x32x16_f16 v[32:47], v[78:81], v[82:85], v[32:47]
	v_add_f32_e32 v82, v88, v87
	v_mul_f32_e32 v83, v200, v200
	v_add_f32_e32 v84, v203, v204
	v_fmac_f32_e32 v83, v198, v198
	v_add_f32_e32 v82, v84, v82
	v_mul_f32_e32 v84, v204, v204
	v_add_f32_e32 v83, v83, v86
	v_fmac_f32_e32 v84, v203, v203
	v_add_f32_e32 v86, v84, v83
	v_add_f32_e32 v83, v223, v224
	v_mfma_f32_32x32x16_f16 v[0:15], v[90:93], v[70:73], v[0:15]
	v_add_f32_e32 v87, v83, v82
	v_mul_f32_e32 v88, v224, v224
	v_fmac_f32_e32 v88, v223, v223
	ds_read_b128 v[82:85], v159 offset:35040
	v_mfma_f32_32x32x16_f16 v[16:31], v[78:81], v[70:73], v[16:31]
	v_add_f32_e32 v71, v225, v226
	v_add_f32_e32 v78, v71, v87
	v_mul_f32_e32 v71, v226, v226
	v_add_f32_e32 v70, v88, v86
	v_fmac_f32_e32 v71, v225, v225
	v_add_f32_e32 v79, v71, v70
	ds_read_b128 v[70:73], v159 offset:43744
	s_waitcnt lgkmcnt(1)
	v_mfma_f32_32x32x16_f16 v[48:63], v[82:85], v[74:77], v[48:63]
	v_add_f32_e32 v80, v227, v228
	v_add_f32_e32 v78, v80, v78
	v_mul_f32_e32 v80, v228, v228
	v_fmac_f32_e32 v80, v227, v227
	v_add_f32_e32 v79, v80, v79
	v_add_f32_e32 v80, v229, v230
	v_add_f32_e32 v78, v80, v78
	v_mfma_f32_32x32x16_f16 v[0:15], v[82:85], v[66:69], v[0:15]
	s_nop 3
	v_cvt_pk_f16_f32 v55, v54, v55
	v_cvt_pk_f16_f32 v54, v52, v53
	v_cvt_pk_f16_f32 v53, v50, v51
	v_cvt_pk_f16_f32 v52, v48, v49
	s_waitcnt vmcnt(3)
	s_waitcnt lgkmcnt(0)
	v_mfma_f32_32x32x16_f16 v[16:31], v[70:73], v[66:69], v[16:31]
	v_lshrrev_b32_e32 v69, 16, v139
	v_mfma_f32_32x32x16_f16 v[32:47], v[70:73], v[74:77], v[32:47]
	v_lshrrev_b32_e32 v70, 8, v139
	v_perm_b32 v69, v70, v69, s4
	v_perm_b32 v66, v240, v138, s42
	v_perm_b32 v67, v240, v138, s43
	v_perm_b32 v68, v240, v139, s42
	v_or_b32_e32 v69, 0x64006400, v69
	v_pk_add_f16 v66, v66, s5 op_sel_hi:[1,0]
	v_pk_add_f16 v67, v67, s5 op_sel_hi:[1,0]
	v_pk_add_f16 v68, v68, s5 op_sel_hi:[1,0]
	v_pk_add_f16 v69, v69, s5 op_sel_hi:[1,0]
	s_nop 1
	v_mfma_f32_32x32x16_f16 v[0:15], v[66:69], v[52:55], v[0:15]
	v_perm_b32 v48, v240, v136, s42
	v_perm_b32 v49, v240, v136, s43
	v_perm_b32 v50, v240, v137, s42
	v_perm_b32 v51, v240, v137, s43
	v_pk_add_f16 v48, v48, s5 op_sel_hi:[1,0]
	v_pk_add_f16 v49, v49, s5 op_sel_hi:[1,0]
	v_pk_add_f16 v50, v50, s5 op_sel_hi:[1,0]
	v_pk_add_f16 v51, v51, s5 op_sel_hi:[1,0]
	v_cvt_pk_f16_f32 v39, v38, v39
	v_cvt_pk_f16_f32 v38, v36, v37
	v_mfma_f32_32x32x16_f16 v[16:31], v[48:51], v[52:55], v[16:31]
	v_perm_b32 v48, v240, v134, s42
	v_perm_b32 v49, v240, v134, s43
	v_perm_b32 v50, v240, v135, s42
	v_perm_b32 v51, v240, v135, s43
	v_pk_add_f16 v48, v48, s5 op_sel_hi:[1,0]
	v_pk_add_f16 v49, v49, s5 op_sel_hi:[1,0]
	v_pk_add_f16 v50, v50, s5 op_sel_hi:[1,0]
	v_pk_add_f16 v51, v51, s5 op_sel_hi:[1,0]
	v_cvt_pk_f16_f32 v55, v62, v63
	v_cvt_pk_f16_f32 v54, v60, v61
	v_cvt_pk_f16_f32 v53, v58, v59
	v_cvt_pk_f16_f32 v52, v56, v57
	s_waitcnt vmcnt(2)
	v_cvt_pk_f16_f32 v37, v34, v35
	v_mfma_f32_32x32x16_f16 v[0:15], v[48:51], v[52:55], v[0:15]
	v_perm_b32 v48, v240, v142, s42
	v_perm_b32 v49, v240, v142, s43
	v_perm_b32 v50, v240, v143, s42
	v_perm_b32 v51, v240, v143, s43
	v_pk_add_f16 v48, v48, s5 op_sel_hi:[1,0]
	v_pk_add_f16 v49, v49, s5 op_sel_hi:[1,0]
	v_pk_add_f16 v50, v50, s5 op_sel_hi:[1,0]
	v_pk_add_f16 v51, v51, s5 op_sel_hi:[1,0]
	v_cvt_pk_f16_f32 v36, v32, v33
	s_waitcnt vmcnt(1)
	v_mfma_f32_32x32x16_f16 v[16:31], v[48:51], v[52:55], v[16:31]
	v_lshrrev_b32_e32 v51, 16, v133
	v_lshrrev_b32_e32 v52, 8, v133
	v_perm_b32 v51, v52, v51, s4
	v_perm_b32 v48, v240, v132, s42
	v_perm_b32 v49, v240, v132, s43
	v_perm_b32 v50, v240, v133, s42
	v_or_b32_e32 v51, 0x64006400, v51
	v_pk_add_f16 v48, v48, s5 op_sel_hi:[1,0]
	v_pk_add_f16 v49, v49, s5 op_sel_hi:[1,0]
	v_pk_add_f16 v50, v50, s5 op_sel_hi:[1,0]
	v_pk_add_f16 v51, v51, s5 op_sel_hi:[1,0]
	s_nop 1
	v_mfma_f32_32x32x16_f16 v[0:15], v[48:51], v[36:39], v[0:15]
	v_perm_b32 v32, v240, v140, s42
	v_perm_b32 v33, v240, v140, s43
	v_perm_b32 v34, v240, v141, s42
	v_perm_b32 v35, v240, v141, s43
	v_pk_add_f16 v32, v32, s5 op_sel_hi:[1,0]
	v_pk_add_f16 v33, v33, s5 op_sel_hi:[1,0]
	v_pk_add_f16 v34, v34, s5 op_sel_hi:[1,0]
	v_pk_add_f16 v35, v35, s5 op_sel_hi:[1,0]
	v_mul_f32_e32 v74, v230, v230
	v_fmac_f32_e32 v74, v229, v229
	v_mfma_f32_32x32x16_f16 v[16:31], v[32:35], v[36:39], v[16:31]
	v_perm_b32 v32, v240, v130, s42
	v_perm_b32 v33, v240, v130, s43
	v_perm_b32 v34, v240, v131, s42
	v_perm_b32 v35, v240, v131, s43
	v_pk_add_f16 v32, v32, s5 op_sel_hi:[1,0]
	v_pk_add_f16 v33, v33, s5 op_sel_hi:[1,0]
	v_pk_add_f16 v34, v34, s5 op_sel_hi:[1,0]
	v_pk_add_f16 v35, v35, s5 op_sel_hi:[1,0]
	v_cvt_pk_f16_f32 v39, v46, v47
	v_cvt_pk_f16_f32 v38, v44, v45
	v_cvt_pk_f16_f32 v37, v42, v43
	v_cvt_pk_f16_f32 v36, v40, v41
	s_waitcnt vmcnt(0)
	v_mul_f32_e32 v76, v232, v232
	v_mfma_f32_32x32x16_f16 v[0:15], v[32:35], v[36:39], v[0:15]
	v_perm_b32 v32, v240, v64, s42
	v_perm_b32 v33, v240, v64, s43
	v_perm_b32 v34, v240, v65, s42
	v_perm_b32 v35, v240, v65, s43
	v_pk_add_f16 v32, v32, s5 op_sel_hi:[1,0]
	v_pk_add_f16 v33, v33, s5 op_sel_hi:[1,0]
	v_pk_add_f16 v34, v34, s5 op_sel_hi:[1,0]
	v_pk_add_f16 v35, v35, s5 op_sel_hi:[1,0]
	s_nop 3
	v_add_f32_e32 v0, v157, v0
	v_add_f32_e32 v74, v74, v79
	v_mfma_f32_32x32x16_f16 v[16:31], v[32:35], v[36:39], v[16:31]
	v_cvt_f16_f32_e32 v33, v0
	v_add_f32_e32 v75, v231, v232
	v_fmac_f32_e32 v76, v231, v231
	v_add_f32_e32 v75, v75, v78
	ds_write_b16 v158, v33 offset:18432
	v_add_f32_e32 v74, v76, v74
	v_add_f32_e32 v76, v233, v234
	s_nop 4
	v_add_f32_e32 v16, v157, v16
	v_add_f32_e32 v32, v0, v16
	v_cvt_f16_f32_e32 v34, v16
	v_mul_f32_e32 v16, v16, v16
	v_fmac_f32_e32 v16, v0, v0
	v_add_f32_e32 v0, v157, v1
	v_add_f32_e32 v1, v157, v17
	v_add_f32_e32 v32, 0, v32
	v_add_f32_e32 v17, v0, v1
	v_add_f32_e32 v17, v17, v32
	v_mul_f32_e32 v32, v1, v1
	v_cvt_f16_f32_e32 v1, v1
	v_fmac_f32_e32 v32, v0, v0
	v_cvt_f16_f32_e32 v33, v0
	v_add_f32_e32 v0, v16, v32
	ds_write_b16 v158, v1 offset:23184
	v_add_f32_e32 v1, v157, v2
	v_add_f32_e32 v2, v157, v18
	v_add_f32_e32 v16, v1, v2
	v_add_f32_e32 v16, v16, v17
	v_mul_f32_e32 v17, v2, v2
	v_cvt_f16_f32_e32 v2, v2
	v_cvt_f16_f32_e32 v18, v1
	v_fmac_f32_e32 v17, v1, v1
	v_add_f32_e32 v1, v157, v3
	ds_write_b16 v158, v2 offset:23328
	v_add_f32_e32 v2, v157, v19
	v_add_f32_e32 v3, v1, v2
	v_add_f32_e32 v3, v3, v16
	v_mul_f32_e32 v16, v2, v2
	v_cvt_f16_f32_e32 v2, v2
	v_add_f32_e32 v0, v17, v0
	v_cvt_f16_f32_e32 v17, v1
	v_fmac_f32_e32 v16, v1, v1
	ds_write_b16 v158, v2 offset:23472
	v_add_f32_e32 v1, v157, v4
	v_add_f32_e32 v2, v157, v20
	v_add_f32_e32 v4, v1, v2
	v_add_f32_e32 v3, v4, v3
	v_mul_f32_e32 v4, v2, v2
	v_cvt_f16_f32_e32 v2, v2
	v_add_f32_e32 v0, v16, v0
	v_cvt_f16_f32_e32 v16, v1
	v_fmac_f32_e32 v4, v1, v1
	ds_write_b16 v158, v2 offset:24192
	v_add_f32_e32 v1, v157, v5
	v_add_f32_e32 v2, v157, v21
	v_add_f32_e32 v0, v4, v0
	v_add_f32_e32 v4, v1, v2
	v_add_f32_e32 v3, v4, v3
	v_mul_f32_e32 v4, v2, v2
	v_cvt_f16_f32_e32 v2, v2
	v_cvt_f16_f32_e32 v5, v1
	v_fmac_f32_e32 v4, v1, v1
	v_add_f32_e32 v1, v157, v6
	ds_write_b16 v158, v2 offset:24336
	v_add_f32_e32 v2, v157, v22
	v_add_f32_e32 v0, v4, v0
	v_add_f32_e32 v4, v1, v2
	v_add_f32_e32 v3, v4, v3
	v_mul_f32_e32 v4, v2, v2
	v_cvt_f16_f32_e32 v2, v2
	ds_write_b16 v158, v5 offset:19728
	v_cvt_f16_f32_e32 v5, v1
	v_fmac_f32_e32 v4, v1, v1
	ds_write_b16 v158, v2 offset:24480
	v_add_f32_e32 v1, v157, v7
	v_add_f32_e32 v2, v157, v23
	v_add_f32_e32 v0, v4, v0
	v_add_f32_e32 v4, v1, v2
	v_add_f32_e32 v3, v4, v3
	v_mul_f32_e32 v4, v2, v2
	v_cvt_f16_f32_e32 v2, v2
	ds_write_b16 v158, v5 offset:19872
	v_cvt_f16_f32_e32 v5, v1
	v_fmac_f32_e32 v4, v1, v1
	ds_write_b16 v158, v2 offset:24624
	v_add_f32_e32 v1, v157, v8
	v_add_f32_e32 v2, v157, v24
	v_add_f32_e32 v0, v4, v0
	v_add_f32_e32 v4, v1, v2
	v_add_f32_e32 v3, v4, v3
	v_mul_f32_e32 v4, v2, v2
	v_cvt_f16_f32_e32 v2, v2
	ds_write_b16 v158, v5 offset:20016
	v_cvt_f16_f32_e32 v5, v1
	v_fmac_f32_e32 v4, v1, v1
	ds_write_b16 v158, v2 offset:25344
	v_add_f32_e32 v1, v157, v9
	v_add_f32_e32 v2, v157, v25
	v_add_f32_e32 v0, v4, v0
	v_add_f32_e32 v4, v1, v2
	v_add_f32_e32 v3, v4, v3
	v_mul_f32_e32 v4, v2, v2
	v_cvt_f16_f32_e32 v2, v2
	ds_write_b16 v158, v5 offset:20736
	v_cvt_f16_f32_e32 v5, v1
	v_fmac_f32_e32 v4, v1, v1
	ds_write_b16 v158, v2 offset:25488
	v_add_f32_e32 v1, v157, v10
	v_add_f32_e32 v2, v157, v26
	v_add_f32_e32 v0, v4, v0
	v_add_f32_e32 v4, v1, v2
	v_add_f32_e32 v3, v4, v3
	v_mul_f32_e32 v4, v2, v2
	v_cvt_f16_f32_e32 v2, v2
	ds_write_b16 v158, v5 offset:20880
	v_cvt_f16_f32_e32 v5, v1
	v_fmac_f32_e32 v4, v1, v1
	ds_write_b16 v158, v2 offset:25632
	v_add_f32_e32 v1, v157, v11
	v_add_f32_e32 v2, v157, v27
	v_add_f32_e32 v0, v4, v0
	v_add_f32_e32 v4, v1, v2
	v_add_f32_e32 v3, v4, v3
	v_mul_f32_e32 v4, v2, v2
	v_cvt_f16_f32_e32 v2, v2
	ds_write_b16 v158, v5 offset:21024
	v_cvt_f16_f32_e32 v5, v1
	v_fmac_f32_e32 v4, v1, v1
	ds_write_b16 v158, v2 offset:25776
	v_add_f32_e32 v1, v157, v12
	v_add_f32_e32 v2, v157, v28
	v_add_f32_e32 v0, v4, v0
	v_add_f32_e32 v4, v1, v2
	v_add_f32_e32 v3, v4, v3
	v_mul_f32_e32 v4, v2, v2
	v_cvt_f16_f32_e32 v2, v2
	ds_write_b16 v158, v5 offset:21168
	v_cvt_f16_f32_e32 v5, v1
	v_fmac_f32_e32 v4, v1, v1
	ds_write_b16 v158, v2 offset:26496
	v_add_f32_e32 v1, v157, v13
	v_add_f32_e32 v2, v157, v29
	v_add_f32_e32 v0, v4, v0
	v_add_f32_e32 v4, v1, v2
	v_add_f32_e32 v3, v4, v3
	v_mul_f32_e32 v4, v2, v2
	v_cvt_f16_f32_e32 v2, v2
	ds_write_b16 v158, v5 offset:21888
	v_cvt_f16_f32_e32 v5, v1
	v_fmac_f32_e32 v4, v1, v1
	ds_write_b16 v158, v2 offset:26640
	v_add_f32_e32 v1, v157, v14
	v_add_f32_e32 v2, v157, v30
	v_add_f32_e32 v0, v4, v0
	v_add_f32_e32 v4, v1, v2
	v_add_f32_e32 v3, v4, v3
	v_cvt_f16_f32_e32 v4, v1
	v_add_f32_e32 v75, v76, v75
	v_mul_f32_e32 v76, v234, v234
	ds_write_b16 v158, v5 offset:22032
	v_mul_f32_e32 v5, v2, v2
	v_fmac_f32_e32 v76, v233, v233
	v_mul_f32_e32 v67, v236, v236
	v_fmac_f32_e32 v5, v1, v1
	v_add_f32_e32 v74, v76, v74
	v_fmac_f32_e32 v67, v235, v235
	v_mul_f32_e32 v57, v238, v238
	v_add_f32_e32 v0, v5, v0
	v_cvt_f16_f32_e32 v5, v2
	v_add_f32_e32 v1, v157, v15
	v_add_f32_e32 v2, v157, v31
	v_add_f32_e32 v76, v235, v236
	v_add_f32_e32 v67, v67, v74
	v_fmac_f32_e32 v57, v237, v237
	v_mul_f32_e32 v50, v145, v145
	ds_write_b16 v158, v4 offset:22176
	v_add_f32_e32 v4, v1, v2
	v_add_f32_e32 v66, v76, v75
	v_add_f32_e32 v56, v237, v238
	v_add_f32_e32 v48, v57, v67
	v_fmac_f32_e32 v50, v144, v144
	v_add_f32_e32 v3, v4, v3
	v_mul_f32_e32 v4, v2, v2
	v_add_f32_e32 v56, v56, v66
	v_add_f32_e32 v49, v144, v145
	v_add_f32_e32 v40, v50, v48
	v_fmac_f32_e32 v4, v1, v1
	v_add_f32_e32 v49, v49, v56
	v_add_f32_e32 v40, v98, v40
	v_add_f32_e32 v4, v4, v0
	v_add_f32_e32 v41, v99, v49
	v_cvt_pk_f16_f32 v6, v1, v2
	v_add_f32_e32 v1, v40, v4
	v_lshlrev_b32_e32 v4, 2, v156
	v_add_f32_e32 v0, v41, v3
	v_xor_b32_e32 v3, 0x80, v4
	s_nop 0
	ds_bpermute_b32 v2, v3, v0
	ds_bpermute_b32 v3, v3, v1
	ds_write_b16 v158, v34 offset:23040
	ds_write_b16 v158, v33 offset:18576
	ds_write_b16 v158, v18 offset:18720
	ds_write_b16 v158, v17 offset:18864
	ds_write_b16 v158, v16 offset:19584
	ds_write_b16 v158, v5 offset:26784
	ds_write_b16 v158, v6 offset:22320
	ds_write_b16_d16_hi v158, v6 offset:26928
	s_and_saveexec_b64 s[0:1], vcc
	s_cbranch_execz .LBB2_26
	s_lshl_b32 s2, s10, 5
	v_lshl_add_u32 v4, s2, 2, v4
	v_or_b32_e32 v5, 0x1e400, v4
	s_waitcnt lgkmcnt(9)
	v_add_f32_e32 v0, v0, v2
	v_add_u32_e32 v4, 0x1e500, v4
	s_waitcnt lgkmcnt(8)
	v_add_f32_e32 v1, v1, v3
	ds_add_f32 v5, v0
	ds_add_f32 v4, v1

.LBB3_24:
	s_or_b64 exec, exec, s[2:3]
	v_and_b32_e32 v1, 31, v0
	v_lshlrev_b32_e32 v2, 2, v1
	v_lshl_or_b32 v2, s13, 7, v2
	v_or_b32_e32 v2, 0x1ee00, v2
	v_lshrrev_b32_e32 v158, 5, v156
	s_waitcnt lgkmcnt(0)
	s_barrier
	s_barrier
	ds_read_b32 v157, v2
	v_mul_u32_u24_e32 v2, 0x88, v1
	s_mul_i32 s0, s16, 0x4400
	v_lshlrev_b32_e32 v2, 1, v2
	v_lshlrev_b32_e32 v3, 4, v158
	v_mov_b32_e32 v138, v0
	v_add3_u32 v159, s0, v2, v3
	ds_read_b128 v[2:5], v159
	ds_read_b128 v[18:21], v159 offset:8704
	ds_read_b128 v[130:133], v159 offset:32
	s_waitcnt vmcnt(10) lgkmcnt(2)
	v_mfma_f32_32x32x16_f16 v[50:65], v[2:5], v[126:129], 0
	s_mov_b32 s2, 0xc060c00
	s_mov_b32 s3, 0xe400
	s_mulk_i32 s16, 0x2400
	s_lshl_b32 s0, s13, 6
	s_or_b32 s0, s16, s0
	s_add_i32 s0, s0, 0x11000
	v_lshl_or_b32 v1, v1, 1, s0
	s_waitcnt lgkmcnt(1)
	v_mfma_f32_32x32x16_f16 v[34:49], v[18:21], v[126:129], 0
	s_or_b32 s0, s10, 2
	s_ashr_i32 s1, s0, 31
	s_lshl_b64 s[0:1], s[0:1], 12
	s_add_u32 s0, s8, s0
	s_addc_u32 s1, s9, s1
	v_cmp_gt_u32_e32 vcc, 32, v156
	v_mfma_f32_32x32x16_f16 v[2:17], v[2:5], v[122:125], 0
	v_mfma_f32_32x32x16_f16 v[18:33], v[18:21], v[122:125], 0
	ds_read_b128 v[134:137], v159 offset:8736
	ds_read_b128 v[160:163], v159 offset:64
	s_waitcnt vmcnt(8) lgkmcnt(2)
	v_mfma_f32_32x32x16_f16 v[50:65], v[130:133], v[118:121], v[50:65]
	s_waitcnt lgkmcnt(1)
	v_mfma_f32_32x32x16_f16 v[34:49], v[134:137], v[118:121], v[34:49]
	v_mfma_f32_32x32x16_f16 v[2:17], v[130:133], v[114:117], v[2:17]
	v_mfma_f32_32x32x16_f16 v[18:33], v[134:137], v[114:117], v[18:33]
	ds_read_b128 v[130:133], v159 offset:8768
	ds_read_b128 v[134:137], v159 offset:96
	s_waitcnt vmcnt(6) lgkmcnt(2)
	v_mfma_f32_32x32x16_f16 v[50:65], v[160:163], v[110:113], v[50:65]
	s_waitcnt lgkmcnt(1)
	v_mfma_f32_32x32x16_f16 v[34:49], v[130:133], v[110:113], v[34:49]
	v_mfma_f32_32x32x16_f16 v[2:17], v[160:163], v[106:109], v[2:17]
	v_mfma_f32_32x32x16_f16 v[18:33], v[130:133], v[106:109], v[18:33]
	ds_read_b128 v[130:133], v159 offset:8800
	ds_read_b128 v[160:163], v159 offset:128
	s_waitcnt vmcnt(4) lgkmcnt(2)
	v_mfma_f32_32x32x16_f16 v[50:65], v[134:137], v[102:105], v[50:65]
	s_waitcnt lgkmcnt(1)
	v_mfma_f32_32x32x16_f16 v[34:49], v[130:133], v[102:105], v[34:49]
	v_mfma_f32_32x32x16_f16 v[2:17], v[134:137], v[98:101], v[2:17]
	v_mfma_f32_32x32x16_f16 v[18:33], v[130:133], v[98:101], v[18:33]
	ds_read_b128 v[130:133], v159 offset:8832
	ds_read_b128 v[134:137], v159 offset:160
	s_waitcnt vmcnt(3) lgkmcnt(2)
	v_mfma_f32_32x32x16_f16 v[50:65], v[160:163], v[94:97], v[50:65]
	s_waitcnt lgkmcnt(1)
	v_mfma_f32_32x32x16_f16 v[34:49], v[130:133], v[94:97], v[34:49]
	v_mfma_f32_32x32x16_f16 v[2:17], v[160:163], v[86:89], v[2:17]
	v_mfma_f32_32x32x16_f16 v[18:33], v[130:133], v[86:89], v[18:33]
	ds_read_b128 v[130:133], v159 offset:8864
	ds_read_b128 v[160:163], v159 offset:192
	s_waitcnt vmcnt(2) lgkmcnt(2)
	v_mfma_f32_32x32x16_f16 v[50:65], v[134:137], v[90:93], v[50:65]
	s_waitcnt lgkmcnt(1)
	v_mfma_f32_32x32x16_f16 v[34:49], v[130:133], v[90:93], v[34:49]
	v_mfma_f32_32x32x16_f16 v[2:17], v[134:137], v[78:81], v[2:17]
	v_mfma_f32_32x32x16_f16 v[18:33], v[130:133], v[78:81], v[18:33]
	ds_read_b128 v[130:133], v159 offset:8896
	ds_read_b128 v[164:167], v159 offset:224
	s_waitcnt vmcnt(1) lgkmcnt(2)
	v_mfma_f32_32x32x16_f16 v[50:65], v[160:163], v[82:85], v[50:65]
	s_waitcnt lgkmcnt(1)
	v_mfma_f32_32x32x16_f16 v[34:49], v[130:133], v[82:85], v[34:49]
	v_mfma_f32_32x32x16_f16 v[2:17], v[160:163], v[70:73], v[2:17]
	v_mfma_f32_32x32x16_f16 v[18:33], v[130:133], v[70:73], v[18:33]
	v_lshlrev_b32_e32 v130, 3, v138
	v_and_b32_e32 v168, 0x1f8, v130
	global_load_dwordx2 v[138:139], v168, s[0:1]
	global_load_dwordx2 v[134:135], v168, s[0:1] offset:512
	global_load_dwordx2 v[132:133], v168, s[0:1] offset:1024
	global_load_dwordx2 v[130:131], v168, s[0:1] offset:1536
	global_load_dwordx2 v[136:137], v168, s[0:1] offset:2048
	s_waitcnt vmcnt(5) lgkmcnt(0)
	v_mfma_f32_32x32x16_f16 v[50:65], v[164:167], v[74:77], v[50:65]
	v_mfma_f32_32x32x16_f16 v[2:17], v[164:167], v[66:69], v[2:17]
	s_nop 10
	v_cvt_pk_f16_f32 v57, v56, v57
	v_cvt_pk_f16_f32 v56, v54, v55
	v_cvt_pk_f16_f32 v55, v52, v53
	v_cvt_pk_f16_f32 v54, v50, v51
	v_perm_b32 v50, v240, v154, s42
	v_perm_b32 v51, v240, v154, s43
	v_perm_b32 v52, v240, v155, s42
	v_perm_b32 v53, v240, v155, s43
	v_pk_add_f16 v50, v50, s3 op_sel_hi:[1,0]
	v_pk_add_f16 v51, v51, s3 op_sel_hi:[1,0]
	v_pk_add_f16 v52, v52, s3 op_sel_hi:[1,0]
	v_pk_add_f16 v53, v53, s3 op_sel_hi:[1,0]
	v_cvt_pk_f16_f32 v65, v64, v65
	v_cvt_pk_f16_f32 v64, v62, v63
	v_cvt_pk_f16_f32 v63, v60, v61
	v_cvt_pk_f16_f32 v62, v58, v59
	v_mfma_f32_32x32x16_f16 v[2:17], v[50:53], v[54:57], v[2:17]
	v_perm_b32 v58, v240, v150, s42
	v_perm_b32 v59, v240, v150, s43
	v_perm_b32 v60, v240, v151, s42
	v_perm_b32 v61, v240, v151, s43
	v_pk_add_f16 v58, v58, s3 op_sel_hi:[1,0]
	v_pk_add_f16 v59, v59, s3 op_sel_hi:[1,0]
	v_pk_add_f16 v60, v60, s3 op_sel_hi:[1,0]
	v_pk_add_f16 v61, v61, s3 op_sel_hi:[1,0]
	s_nop 1
	v_mfma_f32_32x32x16_f16 v[2:17], v[58:61], v[62:65], v[2:17]
	ds_read_b128 v[160:163], v159 offset:8928
	v_perm_b32 v155, v240, v152, s43
	v_perm_b32 v164, v240, v153, s42
	s_waitcnt lgkmcnt(0)
	v_mfma_f32_32x32x16_f16 v[18:33], v[160:163], v[66:69], v[18:33]
	v_perm_b32 v154, v240, v152, s42
	v_perm_b32 v165, v240, v153, s43
	v_pk_add_f16 v152, v154, s3 op_sel_hi:[1,0]
	v_pk_add_f16 v153, v155, s3 op_sel_hi:[1,0]
	v_pk_add_f16 v154, v164, s3 op_sel_hi:[1,0]
	v_pk_add_f16 v155, v165, s3 op_sel_hi:[1,0]
	v_mfma_f32_32x32x16_f16 v[34:49], v[160:163], v[74:77], v[34:49]
	v_perm_b32 v151, v240, v148, s43
	v_perm_b32 v164, v240, v149, s42
	v_mfma_f32_32x32x16_f16 v[18:33], v[152:155], v[54:57], v[18:33]
	v_perm_b32 v150, v240, v148, s42
	v_perm_b32 v165, v240, v149, s43
	v_pk_add_f16 v148, v150, s3 op_sel_hi:[1,0]
	v_pk_add_f16 v149, v151, s3 op_sel_hi:[1,0]
	v_pk_add_f16 v150, v164, s3 op_sel_hi:[1,0]
	v_pk_add_f16 v151, v165, s3 op_sel_hi:[1,0]
	s_nop 2
	v_cvt_pk_f16_f32 v41, v40, v41
	v_cvt_pk_f16_f32 v40, v38, v39
	v_cvt_pk_f16_f32 v38, v34, v35
	v_cvt_pk_f16_f32 v39, v36, v37
	v_mfma_f32_32x32x16_f16 v[18:33], v[148:151], v[62:65], v[18:33]
	v_perm_b32 v34, v240, v146, s42
	v_perm_b32 v35, v240, v146, s43
	v_perm_b32 v36, v240, v147, s42
	v_perm_b32 v37, v240, v147, s43
	v_pk_add_f16 v34, v34, s3 op_sel_hi:[1,0]
	v_pk_add_f16 v35, v35, s3 op_sel_hi:[1,0]
	v_pk_add_f16 v36, v36, s3 op_sel_hi:[1,0]
	v_pk_add_f16 v37, v37, s3 op_sel_hi:[1,0]
	v_perm_b32 v146, v240, v144, s42
	v_perm_b32 v144, v240, v144, s43
	v_perm_b32 v147, v240, v145, s42
	v_perm_b32 v53, v240, v145, s43
	v_pk_add_f16 v50, v146, s3 op_sel_hi:[1,0]
	v_pk_add_f16 v51, v144, s3 op_sel_hi:[1,0]
	v_pk_add_f16 v52, v147, s3 op_sel_hi:[1,0]
	v_pk_add_f16 v53, v53, s3 op_sel_hi:[1,0]
	v_cvt_pk_f16_f32 v49, v48, v49
	v_cvt_pk_f16_f32 v48, v46, v47
	v_cvt_pk_f16_f32 v47, v44, v45
	v_mfma_f32_32x32x16_f16 v[2:17], v[34:37], v[38:41], v[2:17]
	v_cvt_pk_f16_f32 v46, v42, v43
	v_mfma_f32_32x32x16_f16 v[18:33], v[50:53], v[38:41], v[18:33]
	v_perm_b32 v34, v240, v140, s42
	v_perm_b32 v35, v240, v140, s43
	v_perm_b32 v36, v240, v141, s42
	v_perm_b32 v37, v240, v141, s43
	v_perm_b32 v42, v240, v142, s42
	v_perm_b32 v43, v240, v142, s43
	v_perm_b32 v44, v240, v143, s42
	v_perm_b32 v45, v240, v143, s43
	v_pk_add_f16 v34, v34, s3 op_sel_hi:[1,0]
	v_pk_add_f16 v35, v35, s3 op_sel_hi:[1,0]
	v_pk_add_f16 v36, v36, s3 op_sel_hi:[1,0]
	v_pk_add_f16 v37, v37, s3 op_sel_hi:[1,0]
	v_pk_add_f16 v42, v42, s3 op_sel_hi:[1,0]
	v_pk_add_f16 v43, v43, s3 op_sel_hi:[1,0]
	v_pk_add_f16 v44, v44, s3 op_sel_hi:[1,0]
	v_pk_add_f16 v45, v45, s3 op_sel_hi:[1,0]
	v_mfma_f32_32x32x16_f16 v[18:33], v[34:37], v[46:49], v[18:33]
	global_load_dwordx2 v[154:155], v168, s[0:1] offset:2560
	global_load_dwordx2 v[152:153], v168, s[0:1] offset:3072
	global_load_dwordx2 v[150:151], v168, s[0:1] offset:3584
	v_mov_b32_e32 v148, v0
	s_or_b32 s0, s10, 4
	s_ashr_i32 s1, s0, 31
	s_lshl_b64 s[0:1], s[0:1], 12
	v_mfma_f32_32x32x16_f16 v[2:17], v[42:45], v[46:49], v[2:17]
	s_nop 3
	v_add_f32_e32 v196, v157, v18
	v_mul_u32_u24_e32 v18, 0x120, v158
	v_lshl_add_u32 v158, v18, 1, v1
	v_cvt_f16_f32_e32 v1, v196
	v_add_f32_e32 v204, v157, v20
	v_add_f32_e32 v160, v157, v21
	v_add_f32_e32 v162, v157, v22
	s_nop 0
	v_add_f32_e32 v193, v157, v2
	v_add_f32_e32 v198, v157, v3
	v_cvt_pk_f16_f32 v2, v193, v198
	ds_write_b16 v158, v1 offset:4608
	v_add_f32_e32 v203, v157, v4
	v_add_f32_e32 v1, v157, v5
	ds_write_b16 v158, v2
	ds_write_b16_d16_hi v158, v2 offset:144
	v_cvt_pk_f16_f32 v2, v203, v204
	v_cvt_pk_f16_f32 v4, v1, v160
	v_add_f32_e32 v161, v157, v6
	v_add_f32_e32 v163, v157, v7
	v_add_f32_e32 v164, v157, v23
	ds_write_b16 v158, v2 offset:288
	ds_write_b16_d16_hi v158, v2 offset:4896
	ds_write_b16 v158, v4 offset:432
	ds_write_b16_d16_hi v158, v4 offset:5040
	v_cvt_pk_f16_f32 v2, v161, v162
	v_cvt_pk_f16_f32 v4, v163, v164
	v_add_f32_e32 v165, v157, v8
	v_add_f32_e32 v166, v157, v24
	v_add_f32_e32 v167, v157, v9
	v_add_f32_e32 v168, v157, v25
	ds_write_b16 v158, v2 offset:1152
	ds_write_b16_d16_hi v158, v2 offset:5760
	ds_write_b16 v158, v4 offset:1296
	ds_write_b16_d16_hi v158, v4 offset:5904
	v_cvt_pk_f16_f32 v2, v165, v166
	v_cvt_pk_f16_f32 v4, v167, v168
	v_add_f32_e32 v169, v157, v10
	v_add_f32_e32 v170, v157, v26
	v_add_f32_e32 v171, v157, v11
	v_add_f32_e32 v172, v157, v27
	ds_write_b16 v158, v2 offset:1440
	ds_write_b16_d16_hi v158, v2 offset:6048
	ds_write_b16 v158, v4 offset:1584
	ds_write_b16_d16_hi v158, v4 offset:6192
	v_cvt_pk_f16_f32 v2, v169, v170
	v_cvt_pk_f16_f32 v4, v171, v172
	v_add_f32_e32 v173, v157, v12
	v_add_f32_e32 v174, v157, v28
	v_add_f32_e32 v175, v157, v13
	v_add_f32_e32 v176, v157, v29
	ds_write_b16 v158, v2 offset:2304
	ds_write_b16_d16_hi v158, v2 offset:6912
	ds_write_b16 v158, v4 offset:2448
	ds_write_b16_d16_hi v158, v4 offset:7056
	v_cvt_pk_f16_f32 v2, v173, v174
	v_cvt_pk_f16_f32 v4, v175, v176
	v_add_f32_e32 v177, v157, v14
	v_add_f32_e32 v178, v157, v30
	v_add_f32_e32 v179, v157, v15
	v_add_f32_e32 v180, v157, v31
	ds_write_b16 v158, v2 offset:2592
	ds_write_b16_d16_hi v158, v2 offset:7200
	ds_write_b16 v158, v4 offset:2736
	ds_write_b16_d16_hi v158, v4 offset:7344
	v_cvt_pk_f16_f32 v2, v177, v178
	v_cvt_pk_f16_f32 v4, v179, v180
	v_add_f32_e32 v200, v157, v19
	v_add_f32_e32 v181, v157, v16
	v_add_f32_e32 v183, v157, v32
	v_add_f32_e32 v182, v157, v17
	v_add_f32_e32 v184, v157, v33
	v_cvt_pk_f16_f32 v18, v200, v181
	ds_write_b16 v158, v2 offset:3456
	ds_write_b16_d16_hi v158, v2 offset:8064
	ds_write_b16 v158, v4 offset:3600
	ds_write_b16_d16_hi v158, v4 offset:8208
	v_cvt_pk_f16_f32 v3, v183, v182
	v_cvt_f16_f32_e32 v5, v184
	ds_write_b16 v158, v18 offset:4752
	ds_write_b16_d16_hi v158, v18 offset:3744
	ds_write_b16 v158, v3 offset:8352
	ds_write_b16_d16_hi v158, v3 offset:3888
	ds_write_b16 v158, v5 offset:8496
	s_waitcnt lgkmcnt(0)
	s_barrier
	ds_read_b128 v[2:5], v159 offset:34816
	ds_read_b128 v[18:21], v159 offset:43520
	ds_read_b128 v[140:143], v159 offset:34848
	ds_read_b128 v[144:147], v159 offset:43552
	s_waitcnt lgkmcnt(3)
	v_mfma_f32_32x32x16_f16 v[50:65], v[2:5], v[126:129], 0
	s_add_u32 s0, s8, s0
	s_addc_u32 s1, s9, s1
	s_waitcnt lgkmcnt(2)
	v_mfma_f32_32x32x16_f16 v[34:49], v[18:21], v[126:129], 0
	v_mfma_f32_32x32x16_f16 v[2:17], v[2:5], v[122:125], 0
	v_mfma_f32_32x32x16_f16 v[18:33], v[18:21], v[122:125], 0
	ds_read_b128 v[242:245], v159 offset:34880
	ds_read_b128 v[246:249], v159 offset:43584
	s_waitcnt lgkmcnt(3)
	v_mfma_f32_32x32x16_f16 v[50:65], v[140:143], v[118:121], v[50:65]
	s_waitcnt lgkmcnt(2)
	v_mfma_f32_32x32x16_f16 v[34:49], v[144:147], v[118:121], v[34:49]
	v_mfma_f32_32x32x16_f16 v[2:17], v[140:143], v[114:117], v[2:17]
	v_mfma_f32_32x32x16_f16 v[18:33], v[144:147], v[114:117], v[18:33]
	ds_read_b128 v[140:143], v159 offset:34912
	ds_read_b128 v[144:147], v159 offset:43616
	s_waitcnt lgkmcnt(3)
	v_mfma_f32_32x32x16_f16 v[50:65], v[242:245], v[110:113], v[50:65]
	s_waitcnt lgkmcnt(2)
	v_mfma_f32_32x32x16_f16 v[34:49], v[246:249], v[110:113], v[34:49]
	v_mfma_f32_32x32x16_f16 v[2:17], v[242:245], v[106:109], v[2:17]
	v_mfma_f32_32x32x16_f16 v[18:33], v[246:249], v[106:109], v[18:33]
	ds_read_b128 v[242:245], v159 offset:34944
	ds_read_b128 v[246:249], v159 offset:43648
	s_waitcnt lgkmcnt(3)
	v_mfma_f32_32x32x16_f16 v[50:65], v[140:143], v[102:105], v[50:65]
	s_waitcnt lgkmcnt(2)
	v_mfma_f32_32x32x16_f16 v[34:49], v[144:147], v[102:105], v[34:49]
	v_mfma_f32_32x32x16_f16 v[2:17], v[140:143], v[98:101], v[2:17]
	v_mfma_f32_32x32x16_f16 v[18:33], v[144:147], v[98:101], v[18:33]
	ds_read_b128 v[186:189], v159 offset:34976
	ds_read_b128 v[206:209], v159 offset:43680
	s_waitcnt lgkmcnt(3)
	v_mfma_f32_32x32x16_f16 v[50:65], v[242:245], v[94:97], v[50:65]
	s_waitcnt lgkmcnt(2)
	v_mfma_f32_32x32x16_f16 v[34:49], v[246:249], v[94:97], v[34:49]
	v_mfma_f32_32x32x16_f16 v[2:17], v[242:245], v[86:89], v[2:17]
	v_mfma_f32_32x32x16_f16 v[18:33], v[246:249], v[86:89], v[18:33]
	ds_read_b128 v[140:143], v159 offset:35008
	ds_read_b128 v[144:147], v159 offset:43712
	s_waitcnt lgkmcnt(3)
	v_mfma_f32_32x32x16_f16 v[50:65], v[186:189], v[90:93], v[50:65]
	s_waitcnt lgkmcnt(2)
	v_mfma_f32_32x32x16_f16 v[34:49], v[206:209], v[90:93], v[34:49]
	v_mfma_f32_32x32x16_f16 v[2:17], v[186:189], v[78:81], v[2:17]
	v_mfma_f32_32x32x16_f16 v[18:33], v[206:209], v[78:81], v[18:33]
	ds_read_b128 v[186:189], v159 offset:35040
	ds_read_b128 v[206:209], v159 offset:43744
	s_waitcnt lgkmcnt(3)
	v_mfma_f32_32x32x16_f16 v[50:65], v[140:143], v[82:85], v[50:65]
	s_waitcnt lgkmcnt(2)
	v_mfma_f32_32x32x16_f16 v[34:49], v[144:147], v[82:85], v[34:49]
	v_mfma_f32_32x32x16_f16 v[2:17], v[140:143], v[70:73], v[2:17]
	v_lshlrev_b32_e32 v140, 3, v148
	v_and_b32_e32 v185, 0x1f8, v140
	global_load_dwordx2 v[148:149], v185, s[0:1]
	global_load_dwordx2 v[142:143], v185, s[0:1] offset:1024
	global_load_dwordx2 v[140:141], v185, s[0:1] offset:1536
	v_mfma_f32_32x32x16_f16 v[18:33], v[144:147], v[70:73], v[18:33]
	global_load_dwordx2 v[144:145], v185, s[0:1] offset:512
	global_load_dwordx2 v[146:147], v185, s[0:1] offset:2048
	s_waitcnt lgkmcnt(1)
	v_mfma_f32_32x32x16_f16 v[50:65], v[186:189], v[74:77], v[50:65]
	v_mfma_f32_32x32x16_f16 v[2:17], v[186:189], v[66:69], v[2:17]
	s_nop 10
	v_cvt_pk_f16_f32 v57, v56, v57
	v_cvt_pk_f16_f32 v56, v54, v55
	v_cvt_pk_f16_f32 v54, v50, v51
	s_waitcnt vmcnt(12)
	v_cvt_pk_f16_f32 v55, v52, v53
	s_waitcnt vmcnt(8)
	v_perm_b32 v50, v240, v138, s42
	v_perm_b32 v51, v240, v138, s43
	v_perm_b32 v52, v240, v139, s42
	v_perm_b32 v53, v240, v139, s43
	v_perm_b32 v139, v240, v136, s43
	v_pk_add_f16 v50, v50, s3 op_sel_hi:[1,0]
	v_pk_add_f16 v51, v51, s3 op_sel_hi:[1,0]
	v_pk_add_f16 v52, v52, s3 op_sel_hi:[1,0]
	v_pk_add_f16 v53, v53, s3 op_sel_hi:[1,0]
	v_perm_b32 v190, v240, v137, s42
	s_waitcnt lgkmcnt(0)
	v_mfma_f32_32x32x16_f16 v[18:33], v[206:209], v[66:69], v[18:33]
	v_perm_b32 v138, v240, v136, s42
	v_perm_b32 v191, v240, v137, s43
	v_pk_add_f16 v136, v138, s3 op_sel_hi:[1,0]
	v_pk_add_f16 v137, v139, s3 op_sel_hi:[1,0]
	v_pk_add_f16 v138, v190, s3 op_sel_hi:[1,0]
	v_pk_add_f16 v139, v191, s3 op_sel_hi:[1,0]
	v_cvt_pk_f16_f32 v65, v64, v65
	v_cvt_pk_f16_f32 v64, v62, v63
	v_cvt_pk_f16_f32 v63, v60, v61
	v_cvt_pk_f16_f32 v62, v58, v59
	v_mfma_f32_32x32x16_f16 v[34:49], v[206:209], v[74:77], v[34:49]
	v_mfma_f32_32x32x16_f16 v[2:17], v[50:53], v[54:57], v[2:17]
	s_waitcnt vmcnt(7)
	v_perm_b32 v58, v240, v134, s42
	v_perm_b32 v59, v240, v134, s43
	v_perm_b32 v60, v240, v135, s42
	v_perm_b32 v61, v240, v135, s43
	v_pk_add_f16 v58, v58, s3 op_sel_hi:[1,0]
	v_pk_add_f16 v59, v59, s3 op_sel_hi:[1,0]
	v_pk_add_f16 v60, v60, s3 op_sel_hi:[1,0]
	v_pk_add_f16 v61, v61, s3 op_sel_hi:[1,0]
	v_mfma_f32_32x32x16_f16 v[18:33], v[136:139], v[54:57], v[18:33]
	v_perm_b32 v134, v240, v154, s42
	v_perm_b32 v135, v240, v154, s43
	v_perm_b32 v154, v240, v155, s42
	v_perm_b32 v155, v240, v155, s43
	v_pk_add_f16 v210, v134, s3 op_sel_hi:[1,0]
	v_pk_add_f16 v211, v135, s3 op_sel_hi:[1,0]
	v_pk_add_f16 v212, v154, s3 op_sel_hi:[1,0]
	v_pk_add_f16 v213, v155, s3 op_sel_hi:[1,0]
	v_cvt_pk_f16_f32 v41, v40, v41
	v_cvt_pk_f16_f32 v40, v38, v39
	v_cvt_pk_f16_f32 v39, v36, v37
	v_cvt_pk_f16_f32 v38, v34, v35
	v_mfma_f32_32x32x16_f16 v[2:17], v[58:61], v[62:65], v[2:17]
	v_perm_b32 v34, v240, v132, s42
	v_perm_b32 v35, v240, v132, s43
	v_perm_b32 v36, v240, v133, s42
	v_perm_b32 v37, v240, v133, s43
	v_pk_add_f16 v34, v34, s3 op_sel_hi:[1,0]
	v_pk_add_f16 v35, v35, s3 op_sel_hi:[1,0]
	v_pk_add_f16 v36, v36, s3 op_sel_hi:[1,0]
	v_pk_add_f16 v37, v37, s3 op_sel_hi:[1,0]
	s_waitcnt vmcnt(6)
	v_mfma_f32_32x32x16_f16 v[18:33], v[210:213], v[62:65], v[18:33]
	v_perm_b32 v132, v240, v152, s42
	v_perm_b32 v133, v240, v152, s43
	v_perm_b32 v134, v240, v153, s42
	v_perm_b32 v53, v240, v153, s43
	v_pk_add_f16 v50, v132, s3 op_sel_hi:[1,0]
	v_pk_add_f16 v51, v133, s3 op_sel_hi:[1,0]
	v_pk_add_f16 v52, v134, s3 op_sel_hi:[1,0]
	v_pk_add_f16 v53, v53, s3 op_sel_hi:[1,0]
	v_cvt_pk_f16_f32 v49, v48, v49
	v_cvt_pk_f16_f32 v48, v46, v47
	v_cvt_pk_f16_f32 v47, v44, v45
	v_cvt_pk_f16_f32 v46, v42, v43
	v_mfma_f32_32x32x16_f16 v[2:17], v[34:37], v[38:41], v[2:17]
	v_perm_b32 v42, v240, v130, s42
	v_perm_b32 v43, v240, v130, s43
	v_perm_b32 v44, v240, v131, s42
	v_perm_b32 v45, v240, v131, s43
	v_pk_add_f16 v42, v42, s3 op_sel_hi:[1,0]
	v_pk_add_f16 v43, v43, s3 op_sel_hi:[1,0]
	v_pk_add_f16 v44, v44, s3 op_sel_hi:[1,0]
	v_pk_add_f16 v45, v45, s3 op_sel_hi:[1,0]
	s_waitcnt vmcnt(5)
	v_mfma_f32_32x32x16_f16 v[18:33], v[50:53], v[38:41], v[18:33]
	v_perm_b32 v34, v240, v150, s42
	v_perm_b32 v35, v240, v150, s43
	v_perm_b32 v36, v240, v151, s42
	v_perm_b32 v37, v240, v151, s43
	v_pk_add_f16 v34, v34, s3 op_sel_hi:[1,0]
	v_pk_add_f16 v35, v35, s3 op_sel_hi:[1,0]
	v_pk_add_f16 v36, v36, s3 op_sel_hi:[1,0]
	v_pk_add_f16 v37, v37, s3 op_sel_hi:[1,0]
	v_mfma_f32_32x32x16_f16 v[2:17], v[42:45], v[46:49], v[2:17]
	global_load_dwordx2 v[154:155], v185, s[0:1] offset:2560
	global_load_dwordx2 v[152:153], v185, s[0:1] offset:3072
	global_load_dwordx2 v[150:151], v185, s[0:1] offset:3584
	s_or_b32 s0, s10, 6
	s_ashr_i32 s1, s0, 31
	s_lshl_b64 s[0:1], s[0:1], 12
	s_add_u32 s0, s8, s0
	v_mfma_f32_32x32x16_f16 v[18:33], v[34:37], v[46:49], v[18:33]
	s_nop 3
	v_add_f32_e32 v185, v157, v2
	v_add_f32_e32 v187, v157, v3
	v_cvt_pk_f16_f32 v2, v185, v187
	v_add_f32_e32 v189, v157, v4
	v_add_f32_e32 v191, v157, v5
	ds_write_b16 v158, v2 offset:18432
	s_nop 0
	s_nop 0
	v_add_f32_e32 v190, v157, v20
	v_add_f32_e32 v192, v157, v21
	ds_write_b16_d16_hi v158, v2 offset:18576
	v_cvt_pk_f16_f32 v2, v189, v190
	v_cvt_pk_f16_f32 v4, v191, v192
	v_add_f32_e32 v194, v157, v6
	v_add_f32_e32 v195, v157, v22
	v_add_f32_e32 v197, v157, v7
	v_add_f32_e32 v199, v157, v23
	ds_write_b16 v158, v2 offset:18720
	ds_write_b16_d16_hi v158, v2 offset:23328
	ds_write_b16 v158, v4 offset:18864
	ds_write_b16_d16_hi v158, v4 offset:23472
	v_cvt_pk_f16_f32 v2, v194, v195
	v_cvt_pk_f16_f32 v4, v197, v199
	v_add_f32_e32 v201, v157, v8
	v_add_f32_e32 v202, v157, v24
	v_add_f32_e32 v205, v157, v9
	v_add_f32_e32 v206, v157, v25
	ds_write_b16 v158, v2 offset:19584
	ds_write_b16_d16_hi v158, v2 offset:24192
	ds_write_b16 v158, v4 offset:19728
	ds_write_b16_d16_hi v158, v4 offset:24336
	v_cvt_pk_f16_f32 v2, v201, v202
	v_cvt_pk_f16_f32 v4, v205, v206
	v_add_f32_e32 v207, v157, v10
	v_add_f32_e32 v209, v157, v26
	v_add_f32_e32 v208, v157, v11
	v_add_f32_e32 v210, v157, v27
	ds_write_b16 v158, v2 offset:19872
	ds_write_b16_d16_hi v158, v2 offset:24480
	ds_write_b16 v158, v4 offset:20016
	ds_write_b16_d16_hi v158, v4 offset:24624
	v_cvt_pk_f16_f32 v2, v207, v209
	v_cvt_pk_f16_f32 v4, v208, v210
	v_add_f32_e32 v211, v157, v12
	v_add_f32_e32 v212, v157, v28
	v_add_f32_e32 v213, v157, v13
	v_add_f32_e32 v214, v157, v29
	ds_write_b16 v158, v2 offset:20736
	ds_write_b16_d16_hi v158, v2 offset:25344
	ds_write_b16 v158, v4 offset:20880
	ds_write_b16_d16_hi v158, v4 offset:25488
	v_cvt_pk_f16_f32 v2, v211, v212
	v_cvt_pk_f16_f32 v4, v213, v214
	v_add_f32_e32 v215, v157, v14
	v_add_f32_e32 v216, v157, v30
	v_add_f32_e32 v217, v157, v15
	v_add_f32_e32 v218, v157, v31
	ds_write_b16 v158, v2 offset:21024
	ds_write_b16_d16_hi v158, v2 offset:25632
	ds_write_b16 v158, v4 offset:21168
	ds_write_b16_d16_hi v158, v4 offset:25776
	v_cvt_pk_f16_f32 v2, v215, v216
	v_cvt_pk_f16_f32 v4, v217, v218
	v_add_f32_e32 v186, v157, v18
	v_add_f32_e32 v188, v157, v19
	v_add_f32_e32 v219, v157, v16
	v_add_f32_e32 v221, v157, v32
	v_add_f32_e32 v220, v157, v17
	v_add_f32_e32 v222, v157, v33
	v_cvt_pk_f16_f32 v18, v186, v188
	ds_write_b16 v158, v2 offset:21888
	ds_write_b16_d16_hi v158, v2 offset:26496
	ds_write_b16 v158, v4 offset:22032
	ds_write_b16_d16_hi v158, v4 offset:26640
	v_cvt_pk_f16_f32 v2, v219, v221
	v_cvt_pk_f16_f32 v4, v220, v222
	ds_write_b16 v158, v18 offset:23040
	ds_write_b16_d16_hi v158, v18 offset:23184
	ds_write_b16 v158, v2 offset:22176
	ds_write_b16_d16_hi v158, v2 offset:26784
	ds_write_b16 v158, v4 offset:22320
	ds_write_b16_d16_hi v158, v4 offset:26928
	s_waitcnt lgkmcnt(0)
	s_barrier
	ds_read_b128 v[2:5], v159
	ds_read_b128 v[18:21], v159 offset:8704
	s_waitcnt lgkmcnt(1)
	v_mfma_f32_32x32x16_f16 v[50:65], v[2:5], v[126:129], 0
	v_lshlrev_b32_e32 v0, 3, v0
	s_addc_u32 s1, s9, s1
	v_and_b32_e32 v0, 0x1f8, v0
	global_load_dwordx2 v[138:139], v0, s[0:1]
	s_waitcnt lgkmcnt(0)
	v_mfma_f32_32x32x16_f16 v[34:49], v[18:21], v[126:129], 0
	v_mfma_f32_32x32x16_f16 v[2:17], v[2:5], v[122:125], 0
	v_mfma_f32_32x32x16_f16 v[18:33], v[18:21], v[122:125], 0
	ds_read_b128 v[130:133], v159 offset:32
	ds_read_b128 v[134:137], v159 offset:8736
	s_waitcnt lgkmcnt(1)
	v_mfma_f32_32x32x16_f16 v[50:65], v[130:133], v[118:121], v[50:65]
	s_waitcnt lgkmcnt(0)
	v_mfma_f32_32x32x16_f16 v[34:49], v[134:137], v[118:121], v[34:49]
	v_mfma_f32_32x32x16_f16 v[2:17], v[130:133], v[114:117], v[2:17]
	v_mfma_f32_32x32x16_f16 v[18:33], v[134:137], v[114:117], v[18:33]
	ds_read_b128 v[224:227], v159 offset:64
	ds_read_b128 v[228:231], v159 offset:8768
	ds_read_b128 v[130:133], v159 offset:96
	ds_read_b128 v[134:137], v159 offset:8800
	s_waitcnt lgkmcnt(3)
	v_mfma_f32_32x32x16_f16 v[50:65], v[224:227], v[110:113], v[50:65]
	s_waitcnt lgkmcnt(2)
	v_mfma_f32_32x32x16_f16 v[34:49], v[228:231], v[110:113], v[34:49]
	v_mfma_f32_32x32x16_f16 v[2:17], v[224:227], v[106:109], v[2:17]
	v_mfma_f32_32x32x16_f16 v[18:33], v[228:231], v[106:109], v[18:33]
	ds_read_b128 v[224:227], v159 offset:128
	ds_read_b128 v[228:231], v159 offset:8832
	s_waitcnt lgkmcnt(3)
	v_mfma_f32_32x32x16_f16 v[50:65], v[130:133], v[102:105], v[50:65]
	s_waitcnt lgkmcnt(2)
	v_mfma_f32_32x32x16_f16 v[34:49], v[134:137], v[102:105], v[34:49]
	v_mfma_f32_32x32x16_f16 v[2:17], v[130:133], v[98:101], v[2:17]
	v_mfma_f32_32x32x16_f16 v[18:33], v[134:137], v[98:101], v[18:33]
	ds_read_b128 v[130:133], v159 offset:160
	ds_read_b128 v[134:137], v159 offset:8864
	s_waitcnt lgkmcnt(3)
	v_mfma_f32_32x32x16_f16 v[50:65], v[224:227], v[94:97], v[50:65]
	s_waitcnt lgkmcnt(2)
	v_mfma_f32_32x32x16_f16 v[34:49], v[228:231], v[94:97], v[34:49]
	v_mfma_f32_32x32x16_f16 v[2:17], v[224:227], v[86:89], v[2:17]
	v_mfma_f32_32x32x16_f16 v[18:33], v[228:231], v[86:89], v[18:33]
	ds_read_b128 v[224:227], v159 offset:192
	ds_read_b128 v[228:231], v159 offset:8896
	s_waitcnt lgkmcnt(3)
	v_mfma_f32_32x32x16_f16 v[50:65], v[130:133], v[90:93], v[50:65]
	s_waitcnt lgkmcnt(2)
	v_mfma_f32_32x32x16_f16 v[34:49], v[134:137], v[90:93], v[34:49]
	v_mfma_f32_32x32x16_f16 v[2:17], v[130:133], v[78:81], v[2:17]
	v_add_f32_e32 v130, v193, v196
	v_add_f32_e32 v130, 0, v130
	v_add_f32_e32 v132, v198, v200
	v_add_f32_e32 v130, v132, v130
	v_mul_f32_e32 v132, v200, v200
	v_fmac_f32_e32 v132, v198, v198
	v_mul_f32_e32 v131, v196, v196
	v_mfma_f32_32x32x16_f16 v[18:33], v[134:137], v[78:81], v[18:33]
	ds_read_b128 v[232:235], v159 offset:224
	ds_read_b128 v[236:239], v159 offset:8928
	v_fmac_f32_e32 v131, v193, v193
	v_add_f32_e32 v131, v131, v132
	v_add_f32_e32 v132, v203, v204
	v_add_f32_e32 v130, v132, v130
	v_mul_f32_e32 v132, v204, v204
	s_waitcnt lgkmcnt(3)
	v_mfma_f32_32x32x16_f16 v[50:65], v[224:227], v[82:85], v[50:65]
	v_fmac_f32_e32 v132, v203, v203
	v_add_f32_e32 v193, v132, v131
	v_add_f32_e32 v131, v1, v160
	v_add_f32_e32 v196, v131, v130
	global_load_dwordx2 v[134:135], v0, s[0:1] offset:512
	global_load_dwordx2 v[132:133], v0, s[0:1] offset:1024
	global_load_dwordx2 v[130:131], v0, s[0:1] offset:1536
	s_waitcnt lgkmcnt(2)
	v_mfma_f32_32x32x16_f16 v[34:49], v[228:231], v[82:85], v[34:49]
	global_load_dwordx2 v[136:137], v0, s[0:1] offset:2048
	v_mfma_f32_32x32x16_f16 v[2:17], v[224:227], v[70:73], v[2:17]
	v_mfma_f32_32x32x16_f16 v[18:33], v[228:231], v[70:73], v[18:33]
	s_waitcnt lgkmcnt(1)
	v_mfma_f32_32x32x16_f16 v[50:65], v[232:235], v[74:77], v[50:65]
	v_mfma_f32_32x32x16_f16 v[2:17], v[232:235], v[66:69], v[2:17]
	s_nop 10
	v_cvt_pk_f16_f32 v57, v56, v57
	v_cvt_pk_f16_f32 v56, v54, v55
	v_cvt_pk_f16_f32 v54, v50, v51
	s_waitcnt vmcnt(12)
	v_lshlrev_b32_e32 v50, 8, v148
	v_cvt_pk_f16_f32 v55, v52, v53
	v_perm_b32 v50, v50, v148, s2
	v_lshrrev_b32_e32 v51, 16, v148
	v_lshrrev_b32_e32 v52, 8, v148
	v_lshrrev_b32_e32 v53, 16, v149
	v_lshrrev_b32_e32 v148, 8, v149
	v_perm_b32 v51, v52, v51, s2
	v_lshlrev_b32_e32 v52, 8, v149
	v_perm_b32 v53, v148, v53, s2
	s_waitcnt vmcnt(8)
	v_perm_b32 v52, v52, v149, s2
	v_perm_b32 v149, v240, v146, s43
	v_perm_b32 v198, v240, v147, s42
	s_waitcnt lgkmcnt(0)
	v_mfma_f32_32x32x16_f16 v[18:33], v[236:239], v[66:69], v[18:33]
	v_or_b32_e32 v50, 0x64006400, v50
	v_or_b32_e32 v51, 0x64006400, v51
	v_or_b32_e32 v52, 0x64006400, v52
	v_or_b32_e32 v53, 0x64006400, v53
	v_pk_add_f16 v50, v50, s3 op_sel_hi:[1,0]
	v_pk_add_f16 v51, v51, s3 op_sel_hi:[1,0]
	v_pk_add_f16 v52, v52, s3 op_sel_hi:[1,0]
	v_pk_add_f16 v53, v53, s3 op_sel_hi:[1,0]
	v_perm_b32 v148, v240, v146, s42
	v_perm_b32 v200, v240, v147, s43
	v_pk_add_f16 v146, v148, s3 op_sel_hi:[1,0]
	v_pk_add_f16 v147, v149, s3 op_sel_hi:[1,0]
	v_pk_add_f16 v148, v198, s3 op_sel_hi:[1,0]
	v_pk_add_f16 v149, v200, s3 op_sel_hi:[1,0]
	v_cvt_pk_f16_f32 v65, v64, v65
	v_cvt_pk_f16_f32 v64, v62, v63
	v_cvt_pk_f16_f32 v62, v58, v59
	v_cvt_pk_f16_f32 v63, v60, v61
	s_waitcnt vmcnt(7)
	v_mfma_f32_32x32x16_f16 v[34:49], v[236:239], v[74:77], v[34:49]
	v_mfma_f32_32x32x16_f16 v[2:17], v[50:53], v[54:57], v[2:17]
	v_perm_b32 v58, v240, v144, s42
	v_perm_b32 v59, v240, v144, s43
	v_perm_b32 v60, v240, v145, s42
	v_perm_b32 v61, v240, v145, s43
	v_mfma_f32_32x32x16_f16 v[18:33], v[146:149], v[54:57], v[18:33]
	v_pk_add_f16 v58, v58, s3 op_sel_hi:[1,0]
	v_pk_add_f16 v59, v59, s3 op_sel_hi:[1,0]
	v_pk_add_f16 v60, v60, s3 op_sel_hi:[1,0]
	v_pk_add_f16 v61, v61, s3 op_sel_hi:[1,0]
	v_perm_b32 v144, v240, v154, s42
	v_perm_b32 v145, v240, v154, s43
	v_perm_b32 v154, v240, v155, s42
	v_perm_b32 v155, v240, v155, s43
	v_pk_add_f16 v224, v144, s3 op_sel_hi:[1,0]
	v_pk_add_f16 v225, v145, s3 op_sel_hi:[1,0]
	v_pk_add_f16 v226, v154, s3 op_sel_hi:[1,0]
	v_pk_add_f16 v227, v155, s3 op_sel_hi:[1,0]
	v_cvt_pk_f16_f32 v41, v40, v41
	v_cvt_pk_f16_f32 v40, v38, v39
	v_cvt_pk_f16_f32 v39, v36, v37
	v_cvt_pk_f16_f32 v38, v34, v35
	s_waitcnt vmcnt(6)
	v_mfma_f32_32x32x16_f16 v[2:17], v[58:61], v[62:65], v[2:17]
	v_perm_b32 v34, v240, v142, s42
	v_perm_b32 v35, v240, v142, s43
	v_mfma_f32_32x32x16_f16 v[18:33], v[224:227], v[62:65], v[18:33]
	v_perm_b32 v36, v240, v143, s42
	v_perm_b32 v37, v240, v143, s43
	v_pk_add_f16 v34, v34, s3 op_sel_hi:[1,0]
	v_pk_add_f16 v35, v35, s3 op_sel_hi:[1,0]
	v_pk_add_f16 v36, v36, s3 op_sel_hi:[1,0]
	v_pk_add_f16 v37, v37, s3 op_sel_hi:[1,0]
	v_perm_b32 v142, v240, v152, s42
	v_perm_b32 v143, v240, v152, s43
	v_perm_b32 v144, v240, v153, s42
	v_perm_b32 v53, v240, v153, s43
	v_pk_add_f16 v50, v142, s3 op_sel_hi:[1,0]
	v_pk_add_f16 v51, v143, s3 op_sel_hi:[1,0]
	v_pk_add_f16 v52, v144, s3 op_sel_hi:[1,0]
	v_pk_add_f16 v53, v53, s3 op_sel_hi:[1,0]
	v_cvt_pk_f16_f32 v49, v48, v49
	v_cvt_pk_f16_f32 v48, v46, v47
	v_cvt_pk_f16_f32 v47, v44, v45
	v_cvt_pk_f16_f32 v46, v42, v43
	v_mfma_f32_32x32x16_f16 v[2:17], v[34:37], v[38:41], v[2:17]
	s_waitcnt vmcnt(5)
	v_mfma_f32_32x32x16_f16 v[18:33], v[50:53], v[38:41], v[18:33]
	v_perm_b32 v42, v240, v140, s42
	v_perm_b32 v43, v240, v140, s43
	v_perm_b32 v44, v240, v141, s42
	v_perm_b32 v45, v240, v141, s43
	v_perm_b32 v34, v240, v150, s42
	v_perm_b32 v35, v240, v150, s43
	v_perm_b32 v36, v240, v151, s42
	v_perm_b32 v37, v240, v151, s43
	v_pk_add_f16 v42, v42, s3 op_sel_hi:[1,0]
	v_pk_add_f16 v43, v43, s3 op_sel_hi:[1,0]
	v_pk_add_f16 v44, v44, s3 op_sel_hi:[1,0]
	v_pk_add_f16 v45, v45, s3 op_sel_hi:[1,0]
	v_pk_add_f16 v34, v34, s3 op_sel_hi:[1,0]
	v_pk_add_f16 v35, v35, s3 op_sel_hi:[1,0]
	v_pk_add_f16 v36, v36, s3 op_sel_hi:[1,0]
	v_pk_add_f16 v37, v37, s3 op_sel_hi:[1,0]
	v_mfma_f32_32x32x16_f16 v[2:17], v[42:45], v[46:49], v[2:17]
	global_load_dwordx2 v[142:143], v0, s[0:1] offset:2560
	global_load_dwordx2 v[140:141], v0, s[0:1] offset:3072
	global_load_dwordx2 v[64:65], v0, s[0:1] offset:3584
	v_mfma_f32_32x32x16_f16 v[18:33], v[34:37], v[46:49], v[18:33]
	s_nop 7
	v_add_f32_e32 v146, v157, v2
	v_add_f32_e32 v148, v157, v3
	v_cvt_pk_f16_f32 v0, v146, v148
	v_add_f32_e32 v150, v157, v4
	v_add_f32_e32 v152, v157, v5
	ds_write_b16 v158, v0
	v_add_f32_e32 v147, v157, v18
	v_cvt_f16_f32_e32 v2, v147
	v_add_f32_e32 v151, v157, v20
	v_add_f32_e32 v153, v157, v21
	ds_write_b16_d16_hi v158, v0 offset:144
	ds_write_b16 v158, v2 offset:4608
	v_cvt_pk_f16_f32 v0, v150, v151
	v_cvt_pk_f16_f32 v3, v152, v153
	v_add_f32_e32 v154, v157, v6
	v_add_f32_e32 v155, v157, v22
	v_add_f32_e32 v198, v157, v7
	v_add_f32_e32 v200, v157, v23
	ds_write_b16 v158, v0 offset:288
	ds_write_b16_d16_hi v158, v0 offset:4896
	ds_write_b16 v158, v3 offset:432
	ds_write_b16_d16_hi v158, v3 offset:5040
	v_cvt_pk_f16_f32 v0, v154, v155
	v_cvt_pk_f16_f32 v3, v198, v200
	v_add_f32_e32 v203, v157, v8
	v_add_f32_e32 v204, v157, v24
	v_add_f32_e32 v223, v157, v9
	v_add_f32_e32 v224, v157, v25
	ds_write_b16 v158, v0 offset:1152
	ds_write_b16_d16_hi v158, v0 offset:5760
	ds_write_b16 v158, v3 offset:1296
	ds_write_b16_d16_hi v158, v3 offset:5904
	v_cvt_pk_f16_f32 v0, v203, v204
	v_cvt_pk_f16_f32 v3, v223, v224
	v_add_f32_e32 v225, v157, v10
	v_add_f32_e32 v226, v157, v26
	v_add_f32_e32 v227, v157, v11
	v_add_f32_e32 v228, v157, v27
	ds_write_b16 v158, v0 offset:1440
	ds_write_b16_d16_hi v158, v0 offset:6048
	ds_write_b16 v158, v3 offset:1584
	ds_write_b16_d16_hi v158, v3 offset:6192
	v_cvt_pk_f16_f32 v0, v225, v226
	v_cvt_pk_f16_f32 v3, v227, v228
	v_add_f32_e32 v229, v157, v12
	v_add_f32_e32 v230, v157, v28
	v_add_f32_e32 v231, v157, v13
	v_add_f32_e32 v232, v157, v29
	ds_write_b16 v158, v0 offset:2304
	ds_write_b16_d16_hi v158, v0 offset:6912
	ds_write_b16 v158, v3 offset:2448
	ds_write_b16_d16_hi v158, v3 offset:7056
	v_cvt_pk_f16_f32 v0, v229, v230
	v_cvt_pk_f16_f32 v3, v231, v232
	v_add_f32_e32 v233, v157, v14
	v_add_f32_e32 v234, v157, v30
	v_add_f32_e32 v235, v157, v15
	v_add_f32_e32 v236, v157, v31
	ds_write_b16 v158, v0 offset:2592
	ds_write_b16_d16_hi v158, v0 offset:7200
	ds_write_b16 v158, v3 offset:2736
	ds_write_b16_d16_hi v158, v3 offset:7344
	v_cvt_pk_f16_f32 v0, v233, v234
	v_cvt_pk_f16_f32 v3, v235, v236
	v_add_f32_e32 v149, v157, v19
	v_add_f32_e32 v237, v157, v16
	v_add_f32_e32 v238, v157, v32
	v_add_f32_e32 v144, v157, v17
	v_add_f32_e32 v145, v157, v33
	v_cvt_pk_f16_f32 v18, v149, v237
	ds_write_b16 v158, v0 offset:3456
	ds_write_b16_d16_hi v158, v0 offset:8064
	ds_write_b16 v158, v3 offset:3600
	ds_write_b16_d16_hi v158, v3 offset:8208
	v_cvt_pk_f16_f32 v2, v238, v144
	v_cvt_f16_f32_e32 v4, v145
	ds_write_b16 v158, v18 offset:4752
	ds_write_b16_d16_hi v158, v18 offset:3744
	ds_write_b16 v158, v2 offset:8352
	ds_write_b16_d16_hi v158, v2 offset:3888
	ds_write_b16 v158, v4 offset:8496
	s_waitcnt lgkmcnt(0)
	s_barrier
	ds_read_b128 v[16:19], v159 offset:43520
	s_waitcnt lgkmcnt(0)
	v_mfma_f32_32x32x16_f16 v[32:47], v[16:19], v[126:129], 0
	ds_read_b128 v[2:5], v159 offset:34816
	v_mul_f32_e32 v0, v160, v160
	v_fmac_f32_e32 v0, v1, v1
	v_mul_f32_e32 v6, v162, v162
	v_add_f32_e32 v0, v0, v193
	v_add_f32_e32 v1, v161, v162
	v_fmac_f32_e32 v6, v161, v161
	s_waitcnt lgkmcnt(0)
	v_mfma_f32_32x32x16_f16 v[48:63], v[2:5], v[126:129], 0
	ds_read_b128 v[126:129], v159 offset:34848
	v_add_f32_e32 v1, v1, v196
	v_add_f32_e32 v0, v6, v0
	v_add_f32_e32 v6, v163, v164
	v_add_f32_e32 v1, v6, v1
	v_mul_f32_e32 v6, v164, v164
	v_fmac_f32_e32 v6, v163, v163
	v_add_f32_e32 v0, v6, v0
	v_add_f32_e32 v6, v165, v166
	v_add_f32_e32 v1, v6, v1
	v_mul_f32_e32 v6, v166, v166
	v_fmac_f32_e32 v6, v165, v165
	v_add_f32_e32 v20, v6, v0
	v_add_f32_e32 v0, v167, v168
	v_add_f32_e32 v21, v0, v1
	s_waitcnt lgkmcnt(0)
	v_mfma_f32_32x32x16_f16 v[48:63], v[126:129], v[118:121], v[48:63]
	v_mul_f32_e32 v22, v168, v168
	v_fmac_f32_e32 v22, v167, v167
	v_add_f32_e32 v160, v22, v20
	v_add_f32_e32 v20, v169, v170
	v_mul_f32_e32 v162, v170, v170
	v_add_f32_e32 v161, v20, v21
	v_fmac_f32_e32 v162, v169, v169
	v_mfma_f32_32x32x16_f16 v[0:15], v[2:5], v[122:125], 0
	v_mfma_f32_32x32x16_f16 v[0:15], v[126:129], v[114:117], v[0:15]
	v_mfma_f32_32x32x16_f16 v[16:31], v[16:19], v[122:125], 0
	v_add_f32_e32 v123, v171, v172
	v_add_f32_e32 v122, v162, v160
	v_add_f32_e32 v160, v123, v161
	v_mul_f32_e32 v123, v172, v172
	v_fmac_f32_e32 v123, v171, v171
	v_add_f32_e32 v161, v123, v122
	ds_read_b128 v[122:125], v159 offset:43552
	v_add_f32_e32 v162, v173, v174
	v_add_f32_e32 v160, v162, v160
	v_mul_f32_e32 v162, v174, v174
	v_fmac_f32_e32 v162, v173, v173
	s_waitcnt lgkmcnt(0)
	v_mfma_f32_32x32x16_f16 v[32:47], v[122:125], v[118:121], v[32:47]
	v_mul_f32_e32 v118, v176, v176
	v_add_f32_e32 v161, v162, v161
	v_add_f32_e32 v162, v175, v176
	v_fmac_f32_e32 v118, v175, v175
	v_mul_f32_e32 v120, v178, v178
	v_add_f32_e32 v160, v162, v160
	v_add_f32_e32 v118, v118, v161
	v_add_f32_e32 v119, v177, v178
	v_fmac_f32_e32 v120, v177, v177
	v_add_f32_e32 v119, v119, v160
	v_add_f32_e32 v118, v120, v118
	v_add_f32_e32 v120, v179, v180
	v_add_f32_e32 v126, v120, v119
	v_mul_f32_e32 v119, v180, v180
	v_mfma_f32_32x32x16_f16 v[16:31], v[122:125], v[114:117], v[16:31]
	v_add_f32_e32 v114, v181, v183
	v_fmac_f32_e32 v119, v179, v179
	v_add_f32_e32 v122, v114, v126
	v_mul_f32_e32 v114, v183, v183
	v_add_f32_e32 v127, v119, v118
	v_fmac_f32_e32 v114, v181, v181
	ds_read_b128 v[118:121], v159 offset:34880
	v_add_f32_e32 v123, v114, v127
	ds_read_b128 v[114:117], v159 offset:43584
	v_add_f32_e32 v124, v182, v184
	v_add_f32_e32 v122, v124, v122
	v_mul_f32_e32 v124, v184, v184
	v_fmac_f32_e32 v124, v182, v182
	s_waitcnt lgkmcnt(1)
	v_mfma_f32_32x32x16_f16 v[48:63], v[118:121], v[110:113], v[48:63]
	v_add_f32_e32 v123, v124, v123
	v_add_f32_e32 v124, v185, v186
	v_add_f32_e32 v124, 0, v124
	v_add_f32_e32 v122, 0, v122
	s_waitcnt lgkmcnt(0)
	v_mfma_f32_32x32x16_f16 v[32:47], v[114:117], v[110:113], v[32:47]
	v_mul_f32_e32 v110, v186, v186
	v_mul_f32_e32 v112, v188, v188
	v_fmac_f32_e32 v110, v185, v185
	v_add_f32_e32 v111, v187, v188
	v_fmac_f32_e32 v112, v187, v187
	v_add_f32_e32 v111, v111, v124
	v_add_f32_e32 v110, v110, v112
	v_add_f32_e32 v112, v189, v190
	v_mfma_f32_32x32x16_f16 v[0:15], v[118:121], v[106:109], v[0:15]
	v_add_f32_e32 v118, v112, v111
	v_mul_f32_e32 v111, v190, v190
	v_fmac_f32_e32 v111, v189, v189
	v_add_f32_e32 v119, v111, v110
	v_add_f32_e32 v120, v191, v192
	ds_read_b128 v[110:113], v159 offset:34912
	v_mfma_f32_32x32x16_f16 v[16:31], v[114:117], v[106:109], v[16:31]
	v_mul_f32_e32 v107, v192, v192
	v_fmac_f32_e32 v107, v191, v191
	v_add_f32_e32 v106, v120, v118
	v_add_f32_e32 v114, v107, v119
	v_add_f32_e32 v107, v194, v195
	v_add_f32_e32 v115, v107, v106
	ds_read_b128 v[106:109], v159 offset:43616
	v_mul_f32_e32 v116, v195, v195
	v_fmac_f32_e32 v116, v194, v194
	v_add_f32_e32 v114, v116, v114
	v_add_f32_e32 v116, v197, v199
	v_add_f32_e32 v115, v116, v115
	v_mul_f32_e32 v116, v199, v199
	s_waitcnt lgkmcnt(1)
	v_mfma_f32_32x32x16_f16 v[48:63], v[110:113], v[102:105], v[48:63]
	v_fmac_f32_e32 v116, v197, v197
	s_waitcnt lgkmcnt(0)
	v_mfma_f32_32x32x16_f16 v[32:47], v[106:109], v[102:105], v[32:47]
	v_mul_f32_e32 v104, v202, v202
	v_add_f32_e32 v102, v116, v114
	v_add_f32_e32 v103, v201, v202
	v_fmac_f32_e32 v104, v201, v201
	v_add_f32_e32 v103, v103, v115
	v_add_f32_e32 v102, v104, v102
	v_add_f32_e32 v104, v205, v206
	v_add_f32_e32 v103, v104, v103
	v_mul_f32_e32 v104, v206, v206
	v_mfma_f32_32x32x16_f16 v[0:15], v[110:113], v[98:101], v[0:15]
	v_fmac_f32_e32 v104, v205, v205
	v_add_f32_e32 v110, v104, v102
	v_add_f32_e32 v102, v207, v209
	v_add_f32_e32 v111, v102, v103
	ds_read_b128 v[102:105], v159 offset:34944
	v_mfma_f32_32x32x16_f16 v[16:31], v[106:109], v[98:101], v[16:31]
	v_mul_f32_e32 v98, v209, v209
	v_fmac_f32_e32 v98, v207, v207
	v_add_f32_e32 v106, v98, v110
	v_add_f32_e32 v98, v208, v210
	v_add_f32_e32 v107, v98, v111
	ds_read_b128 v[98:101], v159 offset:43648
	v_mul_f32_e32 v108, v210, v210
	v_fmac_f32_e32 v108, v208, v208
	v_add_f32_e32 v106, v108, v106
	v_add_f32_e32 v108, v211, v212
	s_waitcnt lgkmcnt(1)
	v_mfma_f32_32x32x16_f16 v[48:63], v[102:105], v[94:97], v[48:63]
	v_add_f32_e32 v107, v108, v107
	v_mul_f32_e32 v108, v212, v212
	v_fmac_f32_e32 v108, v211, v211
	v_add_f32_e32 v106, v108, v106
	s_waitcnt lgkmcnt(0)
	v_mfma_f32_32x32x16_f16 v[32:47], v[98:101], v[94:97], v[32:47]
	v_add_f32_e32 v94, v213, v214
	v_add_f32_e32 v94, v94, v107
	v_mul_f32_e32 v95, v214, v214
	v_add_f32_e32 v96, v215, v216
	v_fmac_f32_e32 v95, v213, v213
	v_add_f32_e32 v94, v96, v94
	v_mul_f32_e32 v96, v216, v216
	v_add_f32_e32 v95, v95, v106
	v_fmac_f32_e32 v96, v215, v215
	v_mfma_f32_32x32x16_f16 v[0:15], v[102:105], v[86:89], v[0:15]
	v_add_f32_e32 v102, v96, v95
	v_add_f32_e32 v95, v217, v218
	v_add_f32_e32 v103, v95, v94
	ds_read_b128 v[94:97], v159 offset:34976
	v_mul_f32_e32 v104, v218, v218
	v_fmac_f32_e32 v104, v217, v217
	v_mfma_f32_32x32x16_f16 v[16:31], v[98:101], v[86:89], v[16:31]
	v_add_f32_e32 v86, v219, v221
	v_add_f32_e32 v99, v86, v103
	ds_read_b128 v[86:89], v159 offset:43680
	v_mul_f32_e32 v100, v221, v221
	v_add_f32_e32 v98, v104, v102
	v_fmac_f32_e32 v100, v219, v219
	v_add_f32_e32 v98, v100, v98
	s_waitcnt lgkmcnt(1)
	v_mfma_f32_32x32x16_f16 v[48:63], v[94:97], v[90:93], v[48:63]
	v_add_f32_e32 v100, v220, v222
	v_add_f32_e32 v99, v100, v99
	v_mul_f32_e32 v100, v222, v222
	v_fmac_f32_e32 v100, v220, v220
	v_add_f32_e32 v98, v100, v98
	v_add_f32_e32 v98, v123, v98
	v_add_f32_e32 v99, v122, v99
	s_waitcnt lgkmcnt(0)
	v_mfma_f32_32x32x16_f16 v[32:47], v[86:89], v[90:93], v[32:47]
	v_add_f32_e32 v90, v146, v147
	v_add_f32_e32 v90, 0, v90
	v_add_f32_e32 v92, v148, v149
	v_mul_f32_e32 v91, v147, v147
	v_add_f32_e32 v90, v92, v90
	v_mul_f32_e32 v92, v149, v149
	v_fmac_f32_e32 v91, v146, v146
	v_fmac_f32_e32 v92, v148, v148
	v_mfma_f32_32x32x16_f16 v[0:15], v[94:97], v[78:81], v[0:15]
	v_add_f32_e32 v94, v91, v92
	v_add_f32_e32 v91, v150, v151
	v_add_f32_e32 v95, v91, v90
	ds_read_b128 v[90:93], v159 offset:35008
	v_mul_f32_e32 v96, v151, v151
	v_fmac_f32_e32 v96, v150, v150
	v_mfma_f32_32x32x16_f16 v[16:31], v[86:89], v[78:81], v[16:31]
	v_add_f32_e32 v78, v152, v153
	v_add_f32_e32 v87, v78, v95
	ds_read_b128 v[78:81], v159 offset:43712
	v_mul_f32_e32 v88, v153, v153
	v_add_f32_e32 v86, v96, v94
	v_fmac_f32_e32 v88, v152, v152
	v_add_f32_e32 v86, v88, v86
	v_add_f32_e32 v88, v154, v155
	v_add_f32_e32 v87, v88, v87
	v_mul_f32_e32 v88, v155, v155
	v_fmac_f32_e32 v88, v154, v154
	v_add_f32_e32 v86, v88, v86
	v_add_f32_e32 v88, v198, v200
	s_waitcnt lgkmcnt(1)
	v_mfma_f32_32x32x16_f16 v[48:63], v[90:93], v[82:85], v[48:63]
	s_waitcnt lgkmcnt(0)
	v_mfma_f32_32x32x16_f16 v[32:47], v[78:81], v[82:85], v[32:47]
	v_add_f32_e32 v82, v88, v87
	v_mul_f32_e32 v83, v200, v200
	v_add_f32_e32 v84, v203, v204
	v_fmac_f32_e32 v83, v198, v198
	v_add_f32_e32 v82, v84, v82
	v_mul_f32_e32 v84, v204, v204
	v_add_f32_e32 v83, v83, v86
	v_fmac_f32_e32 v84, v203, v203
	v_add_f32_e32 v86, v84, v83
	v_add_f32_e32 v83, v223, v224
	v_mfma_f32_32x32x16_f16 v[0:15], v[90:93], v[70:73], v[0:15]
	v_add_f32_e32 v87, v83, v82
	v_mul_f32_e32 v88, v224, v224
	v_fmac_f32_e32 v88, v223, v223
	ds_read_b128 v[82:85], v159 offset:35040
	v_mfma_f32_32x32x16_f16 v[16:31], v[78:81], v[70:73], v[16:31]
	v_add_f32_e32 v71, v225, v226
	v_add_f32_e32 v78, v71, v87
	v_mul_f32_e32 v71, v226, v226
	v_add_f32_e32 v70, v88, v86
	v_fmac_f32_e32 v71, v225, v225
	v_add_f32_e32 v79, v71, v70
	ds_read_b128 v[70:73], v159 offset:43744
	s_waitcnt lgkmcnt(1)
	v_mfma_f32_32x32x16_f16 v[48:63], v[82:85], v[74:77], v[48:63]
	v_add_f32_e32 v80, v227, v228
	v_add_f32_e32 v78, v80, v78
	v_mul_f32_e32 v80, v228, v228
	v_fmac_f32_e32 v80, v227, v227
	v_add_f32_e32 v79, v80, v79
	v_add_f32_e32 v80, v229, v230
	v_add_f32_e32 v78, v80, v78
	v_mfma_f32_32x32x16_f16 v[0:15], v[82:85], v[66:69], v[0:15]
	s_nop 3
	v_cvt_pk_f16_f32 v55, v54, v55
	v_cvt_pk_f16_f32 v54, v52, v53
	v_cvt_pk_f16_f32 v53, v50, v51
	v_cvt_pk_f16_f32 v52, v48, v49
	s_waitcnt vmcnt(3)
	s_waitcnt lgkmcnt(0)
	v_mfma_f32_32x32x16_f16 v[16:31], v[70:73], v[66:69], v[16:31]
	v_lshrrev_b32_e32 v69, 16, v139
	v_mfma_f32_32x32x16_f16 v[32:47], v[70:73], v[74:77], v[32:47]
	v_lshrrev_b32_e32 v70, 8, v139
	v_perm_b32 v69, v70, v69, s2
	v_perm_b32 v66, v240, v138, s42
	v_perm_b32 v67, v240, v138, s43
	v_perm_b32 v68, v240, v139, s42
	v_or_b32_e32 v69, 0x64006400, v69
	v_pk_add_f16 v66, v66, s3 op_sel_hi:[1,0]
	v_pk_add_f16 v67, v67, s3 op_sel_hi:[1,0]
	v_pk_add_f16 v68, v68, s3 op_sel_hi:[1,0]
	v_pk_add_f16 v69, v69, s3 op_sel_hi:[1,0]
	s_nop 1
	v_mfma_f32_32x32x16_f16 v[0:15], v[66:69], v[52:55], v[0:15]
	v_perm_b32 v48, v240, v136, s42
	v_perm_b32 v49, v240, v136, s43
	v_perm_b32 v50, v240, v137, s42
	v_perm_b32 v51, v240, v137, s43
	v_pk_add_f16 v48, v48, s3 op_sel_hi:[1,0]
	v_pk_add_f16 v49, v49, s3 op_sel_hi:[1,0]
	v_pk_add_f16 v50, v50, s3 op_sel_hi:[1,0]
	v_pk_add_f16 v51, v51, s3 op_sel_hi:[1,0]
	v_cvt_pk_f16_f32 v39, v38, v39
	v_cvt_pk_f16_f32 v38, v36, v37
	v_mfma_f32_32x32x16_f16 v[16:31], v[48:51], v[52:55], v[16:31]
	v_perm_b32 v48, v240, v134, s42
	v_perm_b32 v49, v240, v134, s43
	v_perm_b32 v50, v240, v135, s42
	v_perm_b32 v51, v240, v135, s43
	v_pk_add_f16 v48, v48, s3 op_sel_hi:[1,0]
	v_pk_add_f16 v49, v49, s3 op_sel_hi:[1,0]
	v_pk_add_f16 v50, v50, s3 op_sel_hi:[1,0]
	v_pk_add_f16 v51, v51, s3 op_sel_hi:[1,0]
	v_cvt_pk_f16_f32 v55, v62, v63
	v_cvt_pk_f16_f32 v54, v60, v61
	v_cvt_pk_f16_f32 v53, v58, v59
	v_cvt_pk_f16_f32 v52, v56, v57
	s_waitcnt vmcnt(2)
	v_cvt_pk_f16_f32 v37, v34, v35
	v_mfma_f32_32x32x16_f16 v[0:15], v[48:51], v[52:55], v[0:15]
	v_perm_b32 v48, v240, v142, s42
	v_perm_b32 v49, v240, v142, s43
	v_perm_b32 v50, v240, v143, s42
	v_perm_b32 v51, v240, v143, s43
	v_pk_add_f16 v48, v48, s3 op_sel_hi:[1,0]
	v_pk_add_f16 v49, v49, s3 op_sel_hi:[1,0]
	v_pk_add_f16 v50, v50, s3 op_sel_hi:[1,0]
	v_pk_add_f16 v51, v51, s3 op_sel_hi:[1,0]
	v_cvt_pk_f16_f32 v36, v32, v33
	s_waitcnt vmcnt(1)
	v_mfma_f32_32x32x16_f16 v[16:31], v[48:51], v[52:55], v[16:31]
	v_lshrrev_b32_e32 v51, 16, v133
	v_lshrrev_b32_e32 v52, 8, v133
	v_perm_b32 v51, v52, v51, s2
	v_perm_b32 v48, v240, v132, s42
	v_perm_b32 v49, v240, v132, s43
	v_perm_b32 v50, v240, v133, s42
	v_or_b32_e32 v51, 0x64006400, v51
	v_pk_add_f16 v48, v48, s3 op_sel_hi:[1,0]
	v_pk_add_f16 v49, v49, s3 op_sel_hi:[1,0]
	v_pk_add_f16 v50, v50, s3 op_sel_hi:[1,0]
	v_pk_add_f16 v51, v51, s3 op_sel_hi:[1,0]
	s_nop 1
	v_mfma_f32_32x32x16_f16 v[0:15], v[48:51], v[36:39], v[0:15]
	v_perm_b32 v32, v240, v140, s42
	v_perm_b32 v33, v240, v140, s43
	v_perm_b32 v34, v240, v141, s42
	v_perm_b32 v35, v240, v141, s43
	v_pk_add_f16 v32, v32, s3 op_sel_hi:[1,0]
	v_pk_add_f16 v33, v33, s3 op_sel_hi:[1,0]
	v_pk_add_f16 v34, v34, s3 op_sel_hi:[1,0]
	v_pk_add_f16 v35, v35, s3 op_sel_hi:[1,0]
	v_mul_f32_e32 v74, v230, v230
	v_fmac_f32_e32 v74, v229, v229
	v_mfma_f32_32x32x16_f16 v[16:31], v[32:35], v[36:39], v[16:31]
	v_perm_b32 v32, v240, v130, s42
	v_perm_b32 v33, v240, v130, s43
	v_perm_b32 v34, v240, v131, s42
	v_perm_b32 v35, v240, v131, s43
	v_pk_add_f16 v32, v32, s3 op_sel_hi:[1,0]
	v_pk_add_f16 v33, v33, s3 op_sel_hi:[1,0]
	v_pk_add_f16 v34, v34, s3 op_sel_hi:[1,0]
	v_pk_add_f16 v35, v35, s3 op_sel_hi:[1,0]
	v_cvt_pk_f16_f32 v39, v46, v47
	v_cvt_pk_f16_f32 v38, v44, v45
	v_cvt_pk_f16_f32 v37, v42, v43
	v_cvt_pk_f16_f32 v36, v40, v41
	s_waitcnt vmcnt(0)
	v_mul_f32_e32 v76, v232, v232
	v_mfma_f32_32x32x16_f16 v[0:15], v[32:35], v[36:39], v[0:15]
	v_perm_b32 v32, v240, v64, s42
	v_perm_b32 v33, v240, v64, s43
	v_perm_b32 v34, v240, v65, s42
	v_perm_b32 v35, v240, v65, s43
	v_pk_add_f16 v32, v32, s3 op_sel_hi:[1,0]
	v_pk_add_f16 v33, v33, s3 op_sel_hi:[1,0]
	v_pk_add_f16 v34, v34, s3 op_sel_hi:[1,0]
	v_pk_add_f16 v35, v35, s3 op_sel_hi:[1,0]
	s_nop 3
	v_add_f32_e32 v0, v157, v0
	v_add_f32_e32 v74, v74, v79
	v_mfma_f32_32x32x16_f16 v[16:31], v[32:35], v[36:39], v[16:31]
	v_cvt_f16_f32_e32 v33, v0
	v_add_f32_e32 v75, v231, v232
	v_fmac_f32_e32 v76, v231, v231
	v_add_f32_e32 v75, v75, v78
	ds_write_b16 v158, v33 offset:18432
	v_add_f32_e32 v74, v76, v74
	v_add_f32_e32 v76, v233, v234
	s_nop 4
	v_add_f32_e32 v16, v157, v16
	v_add_f32_e32 v32, v0, v16
	v_cvt_f16_f32_e32 v34, v16
	v_mul_f32_e32 v16, v16, v16
	v_fmac_f32_e32 v16, v0, v0
	v_add_f32_e32 v0, v157, v1
	v_add_f32_e32 v1, v157, v17
	v_add_f32_e32 v32, 0, v32
	v_add_f32_e32 v17, v0, v1
	v_add_f32_e32 v17, v17, v32
	v_mul_f32_e32 v32, v1, v1
	v_cvt_f16_f32_e32 v1, v1
	v_fmac_f32_e32 v32, v0, v0
	v_cvt_f16_f32_e32 v33, v0
	v_add_f32_e32 v0, v16, v32
	ds_write_b16 v158, v1 offset:23184
	v_add_f32_e32 v1, v157, v2
	v_add_f32_e32 v2, v157, v18
	v_add_f32_e32 v16, v1, v2
	v_add_f32_e32 v16, v16, v17
	v_mul_f32_e32 v17, v2, v2
	v_cvt_f16_f32_e32 v2, v2
	v_cvt_f16_f32_e32 v18, v1
	v_fmac_f32_e32 v17, v1, v1
	v_add_f32_e32 v1, v157, v3
	ds_write_b16 v158, v2 offset:23328
	v_add_f32_e32 v2, v157, v19
	v_add_f32_e32 v3, v1, v2
	v_add_f32_e32 v3, v3, v16
	v_mul_f32_e32 v16, v2, v2
	v_cvt_f16_f32_e32 v2, v2
	v_add_f32_e32 v0, v17, v0
	v_cvt_f16_f32_e32 v17, v1
	v_fmac_f32_e32 v16, v1, v1
	ds_write_b16 v158, v2 offset:23472
	v_add_f32_e32 v1, v157, v4
	v_add_f32_e32 v2, v157, v20
	v_add_f32_e32 v4, v1, v2
	v_add_f32_e32 v3, v4, v3
	v_mul_f32_e32 v4, v2, v2
	v_cvt_f16_f32_e32 v2, v2
	v_add_f32_e32 v0, v16, v0
	v_cvt_f16_f32_e32 v16, v1
	v_fmac_f32_e32 v4, v1, v1
	ds_write_b16 v158, v2 offset:24192
	v_add_f32_e32 v1, v157, v5
	v_add_f32_e32 v2, v157, v21
	v_add_f32_e32 v0, v4, v0
	v_add_f32_e32 v4, v1, v2
	v_add_f32_e32 v3, v4, v3
	v_mul_f32_e32 v4, v2, v2
	v_cvt_f16_f32_e32 v2, v2
	v_cvt_f16_f32_e32 v5, v1
	v_fmac_f32_e32 v4, v1, v1
	v_add_f32_e32 v1, v157, v6
	ds_write_b16 v158, v2 offset:24336
	v_add_f32_e32 v2, v157, v22
	v_add_f32_e32 v0, v4, v0
	v_add_f32_e32 v4, v1, v2
	v_add_f32_e32 v3, v4, v3
	v_mul_f32_e32 v4, v2, v2
	v_cvt_f16_f32_e32 v2, v2
	ds_write_b16 v158, v5 offset:19728
	v_cvt_f16_f32_e32 v5, v1
	v_fmac_f32_e32 v4, v1, v1
	ds_write_b16 v158, v2 offset:24480
	v_add_f32_e32 v1, v157, v7
	v_add_f32_e32 v2, v157, v23
	v_add_f32_e32 v0, v4, v0
	v_add_f32_e32 v4, v1, v2
	v_add_f32_e32 v3, v4, v3
	v_mul_f32_e32 v4, v2, v2
	v_cvt_f16_f32_e32 v2, v2
	ds_write_b16 v158, v5 offset:19872
	v_cvt_f16_f32_e32 v5, v1
	v_fmac_f32_e32 v4, v1, v1
	ds_write_b16 v158, v2 offset:24624
	v_add_f32_e32 v1, v157, v8
	v_add_f32_e32 v2, v157, v24
	v_add_f32_e32 v0, v4, v0
	v_add_f32_e32 v4, v1, v2
	v_add_f32_e32 v3, v4, v3
	v_mul_f32_e32 v4, v2, v2
	v_cvt_f16_f32_e32 v2, v2
	ds_write_b16 v158, v5 offset:20016
	v_cvt_f16_f32_e32 v5, v1
	v_fmac_f32_e32 v4, v1, v1
	ds_write_b16 v158, v2 offset:25344
	v_add_f32_e32 v1, v157, v9
	v_add_f32_e32 v2, v157, v25
	v_add_f32_e32 v0, v4, v0
	v_add_f32_e32 v4, v1, v2
	v_add_f32_e32 v3, v4, v3
	v_mul_f32_e32 v4, v2, v2
	v_cvt_f16_f32_e32 v2, v2
	ds_write_b16 v158, v5 offset:20736
	v_cvt_f16_f32_e32 v5, v1
	v_fmac_f32_e32 v4, v1, v1
	ds_write_b16 v158, v2 offset:25488
	v_add_f32_e32 v1, v157, v10
	v_add_f32_e32 v2, v157, v26
	v_add_f32_e32 v0, v4, v0
	v_add_f32_e32 v4, v1, v2
	v_add_f32_e32 v3, v4, v3
	v_mul_f32_e32 v4, v2, v2
	v_cvt_f16_f32_e32 v2, v2
	ds_write_b16 v158, v5 offset:20880
	v_cvt_f16_f32_e32 v5, v1
	v_fmac_f32_e32 v4, v1, v1
	ds_write_b16 v158, v2 offset:25632
	v_add_f32_e32 v1, v157, v11
	v_add_f32_e32 v2, v157, v27
	v_add_f32_e32 v0, v4, v0
	v_add_f32_e32 v4, v1, v2
	v_add_f32_e32 v3, v4, v3
	v_mul_f32_e32 v4, v2, v2
	v_cvt_f16_f32_e32 v2, v2
	ds_write_b16 v158, v5 offset:21024
	v_cvt_f16_f32_e32 v5, v1
	v_fmac_f32_e32 v4, v1, v1
	ds_write_b16 v158, v2 offset:25776
	v_add_f32_e32 v1, v157, v12
	v_add_f32_e32 v2, v157, v28
	v_add_f32_e32 v0, v4, v0
	v_add_f32_e32 v4, v1, v2
	v_add_f32_e32 v3, v4, v3
	v_mul_f32_e32 v4, v2, v2
	v_cvt_f16_f32_e32 v2, v2
	ds_write_b16 v158, v5 offset:21168
	v_cvt_f16_f32_e32 v5, v1
	v_fmac_f32_e32 v4, v1, v1
	ds_write_b16 v158, v2 offset:26496
	v_add_f32_e32 v1, v157, v13
	v_add_f32_e32 v2, v157, v29
	v_add_f32_e32 v0, v4, v0
	v_add_f32_e32 v4, v1, v2
	v_add_f32_e32 v3, v4, v3
	v_mul_f32_e32 v4, v2, v2
	v_cvt_f16_f32_e32 v2, v2
	ds_write_b16 v158, v5 offset:21888
	v_cvt_f16_f32_e32 v5, v1
	v_fmac_f32_e32 v4, v1, v1
	ds_write_b16 v158, v2 offset:26640
	v_add_f32_e32 v1, v157, v14
	v_add_f32_e32 v2, v157, v30
	v_add_f32_e32 v0, v4, v0
	v_add_f32_e32 v4, v1, v2
	v_add_f32_e32 v3, v4, v3
	v_cvt_f16_f32_e32 v4, v1
	v_add_f32_e32 v75, v76, v75
	v_mul_f32_e32 v76, v234, v234
	ds_write_b16 v158, v5 offset:22032
	v_mul_f32_e32 v5, v2, v2
	v_fmac_f32_e32 v76, v233, v233
	v_mul_f32_e32 v67, v236, v236
	v_fmac_f32_e32 v5, v1, v1
	v_add_f32_e32 v74, v76, v74
	v_fmac_f32_e32 v67, v235, v235
	v_mul_f32_e32 v57, v238, v238
	v_add_f32_e32 v0, v5, v0
	v_cvt_f16_f32_e32 v5, v2
	v_add_f32_e32 v1, v157, v15
	v_add_f32_e32 v2, v157, v31
	v_add_f32_e32 v76, v235, v236
	v_add_f32_e32 v67, v67, v74
	v_fmac_f32_e32 v57, v237, v237
	v_mul_f32_e32 v50, v145, v145
	ds_write_b16 v158, v4 offset:22176
	v_add_f32_e32 v4, v1, v2
	v_add_f32_e32 v66, v76, v75
	v_add_f32_e32 v56, v237, v238
	v_add_f32_e32 v48, v57, v67
	v_fmac_f32_e32 v50, v144, v144
	v_add_f32_e32 v3, v4, v3
	v_mul_f32_e32 v4, v2, v2
	v_add_f32_e32 v56, v56, v66
	v_add_f32_e32 v49, v144, v145
	v_add_f32_e32 v40, v50, v48
	v_fmac_f32_e32 v4, v1, v1
	v_add_f32_e32 v49, v49, v56
	v_add_f32_e32 v40, v98, v40
	v_add_f32_e32 v4, v4, v0
	v_add_f32_e32 v41, v99, v49
	v_cvt_pk_f16_f32 v6, v1, v2
	v_add_f32_e32 v1, v40, v4
	v_lshlrev_b32_e32 v4, 2, v156
	v_add_f32_e32 v0, v41, v3
	v_xor_b32_e32 v3, 0x80, v4
	s_nop 0
	ds_bpermute_b32 v2, v3, v0
	ds_bpermute_b32 v3, v3, v1
	ds_write_b16 v158, v34 offset:23040
	ds_write_b16 v158, v33 offset:18576
	ds_write_b16 v158, v18 offset:18720
	ds_write_b16 v158, v17 offset:18864
	ds_write_b16 v158, v16 offset:19584
	ds_write_b16 v158, v5 offset:26784
	ds_write_b16 v158, v6 offset:22320
	ds_write_b16_d16_hi v158, v6 offset:26928
	s_and_saveexec_b64 s[0:1], vcc
	s_cbranch_execz .LBB3_26
	s_lshl_b32 s2, s13, 5
	v_lshl_add_u32 v4, s2, 2, v4
	v_or_b32_e32 v5, 0x1e400, v4
	s_waitcnt lgkmcnt(9)
	v_add_f32_e32 v0, v0, v2
	v_add_u32_e32 v4, 0x1e500, v4
	s_waitcnt lgkmcnt(8)
	v_add_f32_e32 v1, v1, v3
	ds_add_f32 v5, v0
	ds_add_f32 v4, v1
